# map-1 epilogue stash read-backs pipelined (8 in flight); P0 norm: loop-invariant gain loads hoisted
# speedup vs baseline: 1.0104x; 1.0023x over previous
.LBB0_96:
	s_or_b64 exec, exec, s[0:1]
	s_add_i32 s0, s25, 0x26ac0
	s_waitcnt vmcnt(0)
	v_mov_b32_e32 v0, s0
	s_add_i32 s0, s25, 0x26ac4
	s_waitcnt lgkmcnt(0)
	s_barrier
	ds_read_b32 v0, v0
	v_mov_b32_e32 v1, s0
	ds_read_b32 v1, v1
	s_add_i32 s0, s25, 0x26ad0
	s_waitcnt lgkmcnt(1)
	v_readfirstlane_b32 s49, v0
	v_mov_b32_e32 v0, s0
	s_add_i32 s0, s25, 0x26ad4
	s_waitcnt lgkmcnt(0)
	v_readfirstlane_b32 s48, v1
	v_mov_b32_e32 v1, s0
	s_add_i32 s0, s25, 0x26af0
	v_mov_b32_e32 v2, s0
	s_add_i32 s0, s25, 0x26af4
	v_mov_b32_e32 v3, s0
	s_add_i32 s0, s25, 0x26af8
	v_mov_b32_e32 v4, s0
	s_add_i32 s0, s25, 0x26afc
	v_mov_b32_e32 v5, s0
	ds_read_b32 v0, v0
	ds_read_b32 v1, v1
	ds_read_b32 v2, v2
	ds_read_b32 v3, v3
	ds_read_b32 v4, v4
	ds_read_b32 v5, v5
	s_waitcnt lgkmcnt(4)
	v_readfirstlane_b32 s2, v1
	v_readfirstlane_b32 s3, v0
	s_waitcnt lgkmcnt(2)
	v_readfirstlane_b32 s4, v3
	v_readfirstlane_b32 s5, v2
	s_waitcnt lgkmcnt(0)
	v_readfirstlane_b32 s6, v5
	s_cmpk_gt_i32 s24, 0x7fff
	v_readfirstlane_b32 s7, v4
	s_cbranch_scc1 .LBB0_111
	s_add_u32 s50, s8, 0x15a00000
	s_addc_u32 s51, s9, 0
	s_add_u32 s52, s8, 0x9a00000
	v_readlane_b32 s0, v255, 6
	s_addc_u32 s53, s9, 0
	s_lshl_b32 s70, s0, 11
	s_lshl_b32 s10, s0, 2
	v_readlane_b32 s1, v255, 7
	s_mov_b32 s11, s71
	s_cmp_lg_u32 s0, 0
	s_cselect_b64 s[0:1], -1, 0
	s_lshl_b64 s[10:11], s[10:11], 2
	s_add_u32 s12, s7, s10
	s_addc_u32 s13, s6, s11
	s_add_u32 s10, s5, s10
	s_addc_u32 s11, s4, s11
	s_lshl_b64 s[4:5], s[70:71], 2
	s_add_u32 s4, s3, s4
	s_addc_u32 s5, s2, s5
	v_lshl_add_u32 v93, v128, 4, s25
	s_ashr_i32 s25, s24, 31
	s_lshl_b32 s26, s54, 4
	s_lshl_b64 s[28:29], s[24:25], 12
	s_add_u32 s28, s50, s28
	v_lshlrev_b32_e32 v160, 5, v128
	v_and_b32_e32 v1, 7, v129
	s_addc_u32 s29, s51, s29
	s_ashr_i32 s27, s26, 31
	v_lshl_add_u64 v[72:73], s[4:5], 0, v[160:161]
	v_lshlrev_b32_e32 v160, 2, v1
	s_lshl_b64 s[30:31], s[26:27], 12
	s_lshl_b64 s[24:25], s[24:25], 13
	v_lshl_add_u64 v[2:3], s[12:13], 0, v[160:161]
	s_add_u32 s34, s49, s24
	v_lshlrev_b32_e32 v0, 1, v128
	s_mov_b64 s[2:3], 0x1800
	v_lshl_add_u64 v[78:79], v[2:3], 0, -16
	v_lshl_add_u64 v[2:3], s[8:9], 0, v[160:161]
	s_mov_b64 s[8:9], 0x600000
	s_addc_u32 s35, s48, s25
	s_lshl_b32 s24, s38, 4
	v_readlane_b32 s25, v255, 4
	v_lshl_add_u64 v[74:75], v[72:73], 0, s[56:57]
	v_lshl_add_u64 v[76:77], v[72:73], 0, s[2:3]
	v_cmp_gt_u32_e64 s[2:3], 16, v128
	v_cmp_lt_u32_e64 s[4:5], 7, v128
	v_cmp_lt_u32_e64 s[6:7], 3, v1
	v_lshl_add_u64 v[80:81], s[10:11], 0, v[160:161]
	v_lshl_add_u64 v[82:83], v[2:3], 0, s[8:9]
	v_cmp_eq_u32_e64 s[8:9], 0, v1
	v_cmp_eq_u32_e64 s[10:11], 1, v1
	v_cmp_eq_u32_e64 s[12:13], 2, v1
	v_cmp_eq_u32_e64 s[14:15], 3, v1
	v_cmp_eq_u32_e64 s[16:17], 4, v1
	v_cmp_eq_u32_e64 s[18:19], 5, v1
	v_cmp_eq_u32_e64 s[20:21], 6, v1
	v_cmp_eq_u32_e64 s[22:23], 7, v1
	s_lshl_b64 s[36:37], s[26:27], 13
	s_add_i32 s27, s25, s24
	v_lshlrev_b32_e32 v84, 4, v0
	global_load_dwordx4 v[130:133], v[72:73], off offset:16
	global_load_dwordx4 v[134:137], v[72:73], off
	global_load_dwordx4 v[138:141], v[72:73], off offset:2064
	global_load_dwordx4 v[142:145], v[72:73], off offset:2048
	global_load_dwordx4 v[146:149], v[74:75], off offset:16
	global_load_dwordx4 v[150:153], v[74:75], off
	global_load_dwordx4 v[154:157], v[76:77], off offset:16
	global_load_dwordx4 v[162:165], v[76:77], off
	s_waitcnt vmcnt(0)
	s_branch .LBB0_100

.LBB0_103:
	v_fmamk_f32 v65, v69, 0x3a000000, v254
	v_cmp_gt_f32_e32 vcc, s76, v65
	v_mul_f32_e32 v66, 0x4f800000, v65
	s_lshl_b64 s[24:25], s[24:25], 1
	v_cndmask_b32_e32 v65, v65, v66, vcc
	v_sqrt_f32_e32 v66, v65
	s_add_u32 s40, s52, s24
	v_add_f32_e32 v64, v68, v70
	s_addc_u32 s41, s53, s25
	v_add_u32_e32 v67, -1, v66
	v_fma_f32 v68, -v67, v66, v65
	v_cmp_ge_f32_e64 s[24:25], 0, v68
	v_add_u32_e32 v68, 1, v66
	v_fmamk_f32 v64, v64, 0x3a000000, v254
	v_cndmask_b32_e64 v67, v66, v67, s[24:25]
	v_fma_f32 v66, -v68, v66, v65
	v_cmp_lt_f32_e64 s[24:25], 0, v66
	v_lshl_add_u64 v[96:97], s[28:29], 0, v[160:161]
	s_nop 0
	v_cndmask_b32_e64 v66, v67, v68, s[24:25]
	v_mul_f32_e32 v67, 0x37800000, v66
	v_cndmask_b32_e32 v66, v66, v67, vcc
	v_cmp_class_f32_e32 vcc, v65, v229
	s_nop 1
	v_cndmask_b32_e32 v65, v66, v65, vcc
	v_div_scale_f32 v66, s[24:25], v65, v65, 1.0
	v_rcp_f32_e32 v67, v66
	s_nop 0
	v_fma_f32 v68, -v66, v67, 1.0
	v_fmac_f32_e32 v67, v68, v67
	v_div_scale_f32 v68, vcc, 1.0, v65, 1.0
	v_mul_f32_e32 v69, v68, v67
	v_fma_f32 v70, -v66, v69, v68
	v_fmac_f32_e32 v69, v70, v67
	v_fma_f32 v66, -v66, v69, v68
	v_div_fmas_f32 v66, v66, v67, v69
	v_div_fixup_f32 v92, v66, v65, 1.0
	v_cmp_gt_f32_e32 vcc, s76, v64
	v_mul_f32_e32 v65, 0x4f800000, v64
	v_pk_mul_f32 v[48:49], v[48:49], v[92:93] op_sel_hi:[1,0]
	v_cndmask_b32_e32 v64, v64, v65, vcc
	v_sqrt_f32_e32 v65, v64
	v_pk_mul_f32 v[50:51], v[50:51], v[92:93] op_sel_hi:[1,0]
	v_pk_mul_f32 v[28:29], v[28:29], v[92:93] op_sel_hi:[1,0]
	v_pk_mul_f32 v[30:31], v[30:31], v[92:93] op_sel_hi:[1,0]
	v_add_u32_e32 v66, -1, v65
	v_fma_f32 v67, -v66, v65, v64
	v_cmp_ge_f32_e64 s[24:25], 0, v67
	v_add_u32_e32 v67, 1, v65
	v_pk_mul_f32 v[16:17], v[16:17], v[92:93] op_sel_hi:[1,0]
	v_cndmask_b32_e64 v66, v65, v66, s[24:25]
	v_fma_f32 v65, -v67, v65, v64
	v_cmp_lt_f32_e64 s[24:25], 0, v65
	v_pk_mul_f32 v[18:19], v[18:19], v[92:93] op_sel_hi:[1,0]
	v_pk_mul_f32 v[0:1], v[0:1], v[92:93] op_sel_hi:[1,0]
	v_cndmask_b32_e64 v65, v66, v67, s[24:25]
	v_mul_f32_e32 v66, 0x37800000, v65
	v_cndmask_b32_e32 v65, v65, v66, vcc
	v_cmp_class_f32_e32 vcc, v64, v229
	v_pk_mul_f32 v[2:3], v[2:3], v[92:93] op_sel_hi:[1,0]
	s_nop 0
	v_cndmask_b32_e32 v64, v65, v64, vcc
	v_div_scale_f32 v65, s[24:25], v64, v64, 1.0
	v_rcp_f32_e32 v66, v65
	s_brev_b32 s24, 47
	s_mov_b32 s25, -1
	v_lshl_add_u64 v[90:91], v[96:97], 0, s[24:25]
	v_fma_f32 v67, -v65, v66, 1.0
	v_fmac_f32_e32 v66, v67, v66
	v_div_scale_f32 v67, vcc, 1.0, v64, 1.0
	v_mul_f32_e32 v68, v67, v66
	v_fma_f32 v69, -v65, v68, v67
	v_fmac_f32_e32 v68, v69, v66
	v_fma_f32 v65, -v65, v68, v67
	v_div_fmas_f32 v65, v65, v66, v68
	v_div_fixup_f32 v94, v65, v64, 1.0
	v_pk_mul_f32 v[54:55], v[54:55], v[94:95] op_sel_hi:[1,0]
	v_pk_mul_f32 v[52:53], v[52:53], v[94:95] op_sel_hi:[1,0]
	s_brev_b32 s24, 47
	v_pk_mul_f32 v[88:89], v[134:135], v[48:49]
	v_pk_mul_f32 v[86:87], v[136:137], v[50:51]
	v_pk_mul_f32 v[50:51], v[60:61], v[92:93] op_sel_hi:[1,0]
	v_pk_mul_f32 v[60:61], v[136:137], v[54:55]
	v_pk_mul_f32 v[54:55], v[56:57], v[94:95] op_sel_hi:[1,0]
	v_bfe_u32 v56, v88, 16, 1
	v_add3_u32 v56, v88, v56, s75
	v_bfe_u32 v57, v89, 16, 1
	v_lshrrev_b32_e32 v56, 16, v56
	v_add3_u32 v57, v89, v57, s75
	v_and_or_b32 v56, v57, s55, v56
	v_bfe_u32 v57, v86, 16, 1
	v_pk_mul_f32 v[48:49], v[62:63], v[92:93] op_sel_hi:[1,0]
	v_pk_mul_f32 v[62:63], v[134:135], v[52:53]
	v_pk_mul_f32 v[52:53], v[58:59], v[94:95] op_sel_hi:[1,0]
	v_add3_u32 v57, v86, v57, s75
	v_bfe_u32 v58, v87, 16, 1
	v_pk_mul_f32 v[50:51], v[130:131], v[50:51]
	v_lshrrev_b32_e32 v57, 16, v57
	v_add3_u32 v58, v87, v58, s75
	v_and_or_b32 v57, v58, s55, v57
	v_bfe_u32 v58, v50, 16, 1
	v_add3_u32 v58, v50, v58, s75
	v_bfe_u32 v59, v51, 16, 1
	v_pk_mul_f32 v[48:49], v[132:133], v[48:49]
	v_lshrrev_b32_e32 v58, 16, v58
	v_add3_u32 v59, v51, v59, s75
	v_and_or_b32 v58, v59, s55, v58
	v_bfe_u32 v59, v48, 16, 1
	v_pk_mul_f32 v[54:55], v[130:131], v[54:55]
	v_add3_u32 v59, v48, v59, s75
	v_bfe_u32 v64, v49, 16, 1
	v_lshrrev_b32_e32 v59, 16, v59
	v_add3_u32 v64, v49, v64, s75
	v_and_or_b32 v59, v64, s55, v59
	v_bfe_u32 v64, v62, 16, 1
	v_add3_u32 v64, v62, v64, s75
	v_bfe_u32 v65, v63, 16, 1
	v_lshrrev_b32_e32 v64, 16, v64
	v_add3_u32 v65, v63, v65, s75
	v_and_or_b32 v64, v65, s55, v64
	v_bfe_u32 v65, v60, 16, 1
	v_pk_mul_f32 v[52:53], v[132:133], v[52:53]
	v_add3_u32 v65, v60, v65, s75
	v_bfe_u32 v66, v61, 16, 1
	v_lshrrev_b32_e32 v65, 16, v65
	v_add3_u32 v66, v61, v66, s75
	v_and_or_b32 v65, v66, s55, v65
	v_bfe_u32 v66, v54, 16, 1
	v_add3_u32 v66, v54, v66, s75
	v_bfe_u32 v67, v55, 16, 1
	v_lshrrev_b32_e32 v66, 16, v66
	v_add3_u32 v67, v55, v67, s75
	v_and_or_b32 v66, v67, s55, v66
	v_bfe_u32 v67, v52, 16, 1
	v_add3_u32 v67, v52, v67, s75
	v_bfe_u32 v68, v53, 16, 1
	v_lshrrev_b32_e32 v67, 16, v67
	v_add3_u32 v68, v53, v68, s75
	v_and_or_b32 v67, v68, s55, v67
	v_add_co_u32_e32 v68, vcc, s24, v96
	s_nop 1
	v_addc_co_u32_e32 v69, vcc, -1, v97, vcc
	global_store_dwordx4 v[68:69], v[56:59], off
	global_store_dwordx4 v160, v[64:67], s[40:41]
	s_nop 0
	v_pk_mul_f32 v[58:59], v[142:143], v[28:29]
	v_pk_mul_f32 v[28:29], v[34:35], v[92:93] op_sel_hi:[1,0]
	v_pk_mul_f32 v[34:35], v[42:43], v[94:95] op_sel_hi:[1,0]
	v_pk_mul_f32 v[56:57], v[144:145], v[30:31]
	v_pk_mul_f32 v[30:31], v[32:33], v[92:93] op_sel_hi:[1,0]
	v_pk_mul_f32 v[32:33], v[40:41], v[94:95] op_sel_hi:[1,0]
	v_pk_mul_f32 v[40:41], v[144:145], v[34:35]
	v_pk_mul_f32 v[34:35], v[44:45], v[94:95] op_sel_hi:[1,0]
	v_bfe_u32 v44, v58, 16, 1
	v_add3_u32 v44, v58, v44, s75
	v_bfe_u32 v45, v59, 16, 1
	v_lshrrev_b32_e32 v44, 16, v44
	v_add3_u32 v45, v59, v45, s75
	v_and_or_b32 v44, v45, s55, v44
	v_bfe_u32 v45, v56, 16, 1
	v_pk_mul_f32 v[42:43], v[142:143], v[32:33]
	v_pk_mul_f32 v[32:33], v[46:47], v[94:95] op_sel_hi:[1,0]
	v_add3_u32 v45, v56, v45, s75
	v_bfe_u32 v46, v57, 16, 1
	v_pk_mul_f32 v[30:31], v[138:139], v[30:31]
	v_lshrrev_b32_e32 v45, 16, v45
	v_add3_u32 v46, v57, v46, s75
	v_and_or_b32 v45, v46, s55, v45
	v_bfe_u32 v46, v30, 16, 1
	v_add3_u32 v46, v30, v46, s75
	v_bfe_u32 v47, v31, 16, 1
	v_pk_mul_f32 v[28:29], v[140:141], v[28:29]
	v_lshrrev_b32_e32 v46, 16, v46
	v_add3_u32 v47, v31, v47, s75
	v_and_or_b32 v46, v47, s55, v46
	v_bfe_u32 v47, v28, 16, 1
	v_pk_mul_f32 v[34:35], v[138:139], v[34:35]
	v_add3_u32 v47, v28, v47, s75
	v_bfe_u32 v64, v29, 16, 1
	v_lshrrev_b32_e32 v47, 16, v47
	v_add3_u32 v64, v29, v64, s75
	v_and_or_b32 v47, v64, s55, v47
	v_bfe_u32 v64, v42, 16, 1
	v_add3_u32 v64, v42, v64, s75
	v_bfe_u32 v65, v43, 16, 1
	v_lshrrev_b32_e32 v64, 16, v64
	v_add3_u32 v65, v43, v65, s75
	v_and_or_b32 v64, v65, s55, v64
	v_bfe_u32 v65, v40, 16, 1
	v_pk_mul_f32 v[32:33], v[140:141], v[32:33]
	v_add3_u32 v65, v40, v65, s75
	v_bfe_u32 v66, v41, 16, 1
	v_lshrrev_b32_e32 v65, 16, v65
	v_add3_u32 v66, v41, v66, s75
	v_and_or_b32 v65, v66, s55, v65
	v_bfe_u32 v66, v34, 16, 1
	v_add3_u32 v66, v34, v66, s75
	v_bfe_u32 v67, v35, 16, 1
	v_lshrrev_b32_e32 v66, 16, v66
	v_add3_u32 v67, v35, v67, s75
	v_and_or_b32 v66, v67, s55, v66
	v_bfe_u32 v67, v32, 16, 1
	v_add3_u32 v67, v32, v67, s75
	v_bfe_u32 v68, v33, 16, 1
	v_lshrrev_b32_e32 v67, 16, v67
	v_add3_u32 v68, v33, v68, s75
	v_and_or_b32 v67, v68, s55, v67
	global_store_dwordx4 v[90:91], v[44:47], off offset:1024
	global_store_dwordx4 v160, v[64:67], s[40:41] offset:1024
	s_nop 0
	v_pk_mul_f32 v[46:47], v[150:151], v[16:17]
	v_pk_mul_f32 v[16:17], v[22:23], v[92:93] op_sel_hi:[1,0]
	v_pk_mul_f32 v[22:23], v[26:27], v[94:95] op_sel_hi:[1,0]
	v_pk_mul_f32 v[44:45], v[152:153], v[18:19]
	v_pk_mul_f32 v[18:19], v[20:21], v[92:93] op_sel_hi:[1,0]
	v_pk_mul_f32 v[20:21], v[24:25], v[94:95] op_sel_hi:[1,0]
	v_pk_mul_f32 v[24:25], v[152:153], v[22:23]
	v_pk_mul_f32 v[22:23], v[36:37], v[94:95] op_sel_hi:[1,0]
	v_bfe_u32 v36, v46, 16, 1
	v_add3_u32 v36, v46, v36, s75
	v_bfe_u32 v37, v47, 16, 1
	v_lshrrev_b32_e32 v36, 16, v36
	v_add3_u32 v37, v47, v37, s75
	v_and_or_b32 v36, v37, s55, v36
	v_bfe_u32 v37, v44, 16, 1
	v_pk_mul_f32 v[26:27], v[150:151], v[20:21]
	v_pk_mul_f32 v[20:21], v[38:39], v[94:95] op_sel_hi:[1,0]
	v_add3_u32 v37, v44, v37, s75
	v_bfe_u32 v38, v45, 16, 1
	v_pk_mul_f32 v[18:19], v[18:19], v[146:147]
	v_lshrrev_b32_e32 v37, 16, v37
	v_add3_u32 v38, v45, v38, s75
	v_and_or_b32 v37, v38, s55, v37
	v_bfe_u32 v38, v18, 16, 1
	v_add3_u32 v38, v18, v38, s75
	v_bfe_u32 v39, v19, 16, 1
	v_pk_mul_f32 v[16:17], v[16:17], v[148:149]
	v_lshrrev_b32_e32 v38, 16, v38
	v_add3_u32 v39, v19, v39, s75
	v_and_or_b32 v38, v39, s55, v38
	v_bfe_u32 v39, v16, 16, 1
	v_pk_mul_f32 v[22:23], v[146:147], v[22:23]
	v_add3_u32 v39, v16, v39, s75
	v_bfe_u32 v64, v17, 16, 1
	v_lshrrev_b32_e32 v39, 16, v39
	v_add3_u32 v64, v17, v64, s75
	v_and_or_b32 v39, v64, s55, v39
	v_bfe_u32 v64, v26, 16, 1
	v_add3_u32 v64, v26, v64, s75
	v_bfe_u32 v65, v27, 16, 1
	v_lshrrev_b32_e32 v64, 16, v64
	v_add3_u32 v65, v27, v65, s75
	v_and_or_b32 v64, v65, s55, v64
	v_bfe_u32 v65, v24, 16, 1
	v_pk_mul_f32 v[20:21], v[148:149], v[20:21]
	v_add3_u32 v65, v24, v65, s75
	v_bfe_u32 v66, v25, 16, 1
	v_lshrrev_b32_e32 v65, 16, v65
	v_add3_u32 v66, v25, v66, s75
	v_and_or_b32 v65, v66, s55, v65
	v_bfe_u32 v66, v22, 16, 1
	v_add3_u32 v66, v22, v66, s75
	v_bfe_u32 v67, v23, 16, 1
	v_lshrrev_b32_e32 v66, 16, v66
	v_add3_u32 v67, v23, v67, s75
	v_and_or_b32 v66, v67, s55, v66
	v_bfe_u32 v67, v20, 16, 1
	v_add3_u32 v67, v20, v67, s75
	v_bfe_u32 v68, v21, 16, 1
	v_lshrrev_b32_e32 v67, 16, v67
	v_add3_u32 v68, v21, v68, s75
	v_and_or_b32 v67, v68, s55, v67
	global_store_dwordx4 v[90:91], v[36:39], off offset:2048
	global_store_dwordx4 v160, v[64:67], s[40:41] offset:2048
	s_nop 0
	v_pk_mul_f32 v[36:37], v[2:3], v[164:165]
	v_pk_mul_f32 v[38:39], v[0:1], v[162:163]
	v_pk_mul_f32 v[2:3], v[4:5], v[92:93] op_sel_hi:[1,0]
	v_pk_mul_f32 v[0:1], v[6:7], v[92:93] op_sel_hi:[1,0]
	v_pk_mul_f32 v[6:7], v[14:15], v[94:95] op_sel_hi:[1,0]
	v_pk_mul_f32 v[4:5], v[2:3], v[154:155]
	v_pk_mul_f32 v[2:3], v[12:13], v[94:95] op_sel_hi:[1,0]
	v_pk_mul_f32 v[12:13], v[6:7], v[164:165]
	v_pk_mul_f32 v[6:7], v[8:9], v[94:95] op_sel_hi:[1,0]
	v_bfe_u32 v8, v38, 16, 1
	v_add3_u32 v8, v38, v8, s75
	v_bfe_u32 v9, v39, 16, 1
	v_lshrrev_b32_e32 v8, 16, v8
	v_add3_u32 v9, v39, v9, s75
	v_and_or_b32 v8, v9, s55, v8
	v_bfe_u32 v9, v36, 16, 1
	v_pk_mul_f32 v[14:15], v[2:3], v[162:163]
	v_pk_mul_f32 v[2:3], v[10:11], v[94:95] op_sel_hi:[1,0]
	v_add3_u32 v9, v36, v9, s75
	v_bfe_u32 v10, v37, 16, 1
	v_lshrrev_b32_e32 v9, 16, v9
	v_add3_u32 v10, v37, v10, s75
	v_and_or_b32 v9, v10, s55, v9
	v_bfe_u32 v10, v4, 16, 1
	v_add3_u32 v10, v4, v10, s75
	v_bfe_u32 v11, v5, 16, 1
	v_pk_mul_f32 v[0:1], v[0:1], v[156:157]
	v_lshrrev_b32_e32 v10, 16, v10
	v_add3_u32 v11, v5, v11, s75
	v_and_or_b32 v10, v11, s55, v10
	v_bfe_u32 v11, v0, 16, 1
	v_pk_mul_f32 v[6:7], v[6:7], v[154:155]
	v_add3_u32 v11, v0, v11, s75
	v_bfe_u32 v64, v1, 16, 1
	v_lshrrev_b32_e32 v11, 16, v11
	v_add3_u32 v64, v1, v64, s75
	v_and_or_b32 v11, v64, s55, v11
	v_bfe_u32 v64, v14, 16, 1
	v_add3_u32 v64, v14, v64, s75
	v_bfe_u32 v65, v15, 16, 1
	v_lshrrev_b32_e32 v64, 16, v64
	v_add3_u32 v65, v15, v65, s75
	v_and_or_b32 v64, v65, s55, v64
	v_bfe_u32 v65, v12, 16, 1
	v_pk_mul_f32 v[2:3], v[2:3], v[156:157]
	v_add3_u32 v65, v12, v65, s75
	v_bfe_u32 v66, v13, 16, 1
	v_lshrrev_b32_e32 v65, 16, v65
	v_add3_u32 v66, v13, v66, s75
	v_and_or_b32 v65, v66, s55, v65
	v_bfe_u32 v66, v6, 16, 1
	v_add3_u32 v66, v6, v66, s75
	v_bfe_u32 v67, v7, 16, 1
	v_lshrrev_b32_e32 v66, 16, v66
	v_add3_u32 v67, v7, v67, s75
	v_and_or_b32 v66, v67, s55, v66
	v_bfe_u32 v67, v2, 16, 1
	v_add3_u32 v67, v2, v67, s75
	v_bfe_u32 v68, v3, 16, 1
	v_lshrrev_b32_e32 v67, 16, v67
	v_add3_u32 v68, v3, v68, s75
	v_and_or_b32 v67, v68, s55, v67
	global_store_dwordx4 v[90:91], v[8:11], off offset:3072
	global_store_dwordx4 v160, v[64:67], s[40:41] offset:3072
	ds_read_b128 v[8:11], v93
	ds_read_b128 v[94:97], v93 offset:24576
	s_waitcnt lgkmcnt(0)
	v_mul_f32_e32 v64, v89, v9
	v_mul_f32_e32 v9, v63, v9
	v_fmac_f32_e32 v64, v88, v8
	v_fmac_f32_e32 v9, v62, v8
	v_mul_f32_e32 v8, v61, v11
	v_mul_f32_e32 v65, v87, v11
	v_fmac_f32_e32 v8, v60, v10
	v_fmac_f32_e32 v65, v86, v10
	v_add_f32_e32 v8, v9, v8
	v_add_f32_e32 v64, v64, v65
	v_add_f32_e32 v65, 0, v8
	ds_read_b128 v[8:11], v93 offset:1024
	v_add_f32_e32 v64, 0, v64
	s_waitcnt lgkmcnt(0)
	v_mul_f32_e32 v66, v51, v9
	v_mul_f32_e32 v9, v55, v9
	v_fmac_f32_e32 v66, v50, v8
	v_fmac_f32_e32 v9, v54, v8
	v_mul_f32_e32 v8, v53, v11
	v_fmac_f32_e32 v8, v52, v10
	v_mul_f32_e32 v67, v49, v11
	v_add_f32_e32 v8, v9, v8
	v_fmac_f32_e32 v67, v48, v10
	v_add_f32_e32 v65, v65, v8
	ds_read_b128 v[8:11], v93 offset:2048
	v_add_f32_e32 v66, v66, v67
	v_add_f32_e32 v64, v64, v66
	s_waitcnt lgkmcnt(0)
	v_mul_f32_e32 v66, v59, v9
	v_mul_f32_e32 v9, v43, v9
	v_fmac_f32_e32 v66, v58, v8
	v_fmac_f32_e32 v9, v42, v8
	v_mul_f32_e32 v8, v41, v11
	v_fmac_f32_e32 v8, v40, v10
	v_mul_f32_e32 v67, v57, v11
	v_add_f32_e32 v8, v9, v8
	v_fmac_f32_e32 v67, v56, v10
	v_add_f32_e32 v65, v65, v8
	ds_read_b128 v[8:11], v93 offset:3072
	v_add_f32_e32 v66, v66, v67
	v_add_f32_e32 v64, v64, v66
	s_waitcnt lgkmcnt(0)
	v_mul_f32_e32 v66, v31, v9
	v_mul_f32_e32 v9, v35, v9
	v_fmac_f32_e32 v66, v30, v8
	v_fmac_f32_e32 v9, v34, v8
	v_mul_f32_e32 v8, v33, v11
	v_fmac_f32_e32 v8, v32, v10
	v_mul_f32_e32 v67, v29, v11
	v_add_f32_e32 v8, v9, v8
	v_fmac_f32_e32 v67, v28, v10
	v_add_f32_e32 v65, v65, v8
	ds_read_b128 v[8:11], v93 offset:4096
	v_add_f32_e32 v66, v66, v67
	v_add_f32_e32 v64, v64, v66
	s_waitcnt lgkmcnt(0)
	v_mul_f32_e32 v66, v47, v9
	v_mul_f32_e32 v9, v27, v9
	v_fmac_f32_e32 v66, v46, v8
	v_fmac_f32_e32 v9, v26, v8
	v_mul_f32_e32 v8, v25, v11
	v_fmac_f32_e32 v8, v24, v10
	v_mul_f32_e32 v67, v45, v11
	v_add_f32_e32 v8, v9, v8
	v_fmac_f32_e32 v67, v44, v10
	v_add_f32_e32 v65, v65, v8
	ds_read_b128 v[8:11], v93 offset:5120
	v_add_f32_e32 v66, v66, v67
	v_add_f32_e32 v64, v64, v66
	s_waitcnt lgkmcnt(0)
	v_mul_f32_e32 v66, v19, v9
	v_mul_f32_e32 v9, v23, v9
	v_fmac_f32_e32 v66, v18, v8
	v_fmac_f32_e32 v9, v22, v8
	v_mul_f32_e32 v8, v21, v11
	v_fmac_f32_e32 v8, v20, v10
	v_mul_f32_e32 v67, v17, v11
	v_add_f32_e32 v8, v9, v8
	v_fmac_f32_e32 v67, v16, v10
	v_add_f32_e32 v65, v65, v8
	ds_read_b128 v[8:11], v93 offset:6144
	v_add_f32_e32 v66, v66, v67
	v_add_f32_e32 v64, v64, v66
	s_waitcnt lgkmcnt(0)
	v_mul_f32_e32 v66, v39, v9
	v_mul_f32_e32 v9, v15, v9
	v_fmac_f32_e32 v66, v38, v8
	v_fmac_f32_e32 v9, v14, v8
	v_mul_f32_e32 v8, v13, v11
	v_fmac_f32_e32 v8, v12, v10
	v_mul_f32_e32 v67, v37, v11
	v_add_f32_e32 v8, v9, v8
	v_fmac_f32_e32 v67, v36, v10
	v_add_f32_e32 v65, v65, v8
	ds_read_b128 v[8:11], v93 offset:7168
	v_add_f32_e32 v66, v66, v67
	v_add_f32_e32 v64, v64, v66
	s_waitcnt lgkmcnt(0)
	v_mul_f32_e32 v66, v5, v9
	v_mul_f32_e32 v67, v1, v11
	v_mul_f32_e32 v9, v7, v9
	v_fmac_f32_e32 v66, v4, v8
	v_fmac_f32_e32 v67, v0, v10
	v_fmac_f32_e32 v9, v6, v8
	v_mul_f32_e32 v8, v3, v11
	v_add_f32_e32 v66, v66, v67
	v_fmac_f32_e32 v8, v2, v10
	v_add_f32_e32 v64, v64, v66
	v_add_f32_e32 v8, v9, v8
	v_add_f32_e32 v10, v65, v8
	ds_swizzle_b32 v8, v64 offset:swizzle(SWAP,1)
	ds_swizzle_b32 v11, v10 offset:swizzle(SWAP,1)
	s_waitcnt lgkmcnt(1)
	v_add_f32_e32 v8, v64, v8
	ds_read_b128 v[64:67], v93 offset:8192
	s_waitcnt lgkmcnt(1)
	v_add_f32_e32 v10, v10, v11
	ds_swizzle_b32 v9, v8 offset:swizzle(SWAP,2)
	ds_swizzle_b32 v11, v10 offset:swizzle(SWAP,2)
	s_waitcnt lgkmcnt(2)
	v_mul_f32_e32 v68, v89, v65
	v_mul_f32_e32 v65, v63, v65
	v_fmac_f32_e32 v68, v88, v64
	v_fmac_f32_e32 v65, v62, v64
	v_mul_f32_e32 v64, v61, v67
	v_mul_f32_e32 v69, v87, v67
	v_fmac_f32_e32 v64, v60, v66
	v_fmac_f32_e32 v69, v86, v66
	v_add_f32_e32 v64, v65, v64
	v_add_f32_e32 v68, v68, v69
	v_add_f32_e32 v69, 0, v64
	ds_read_b128 v[64:67], v93 offset:9216
	v_add_f32_e32 v68, 0, v68
	s_waitcnt lgkmcnt(2)
	v_add_f32_e32 v8, v8, v9
	s_waitcnt lgkmcnt(1)
	v_add_f32_e32 v10, v10, v11
	ds_swizzle_b32 v9, v8 offset:swizzle(SWAP,4)
	s_waitcnt lgkmcnt(1)
	v_mul_f32_e32 v70, v51, v65
	v_mul_f32_e32 v65, v55, v65
	v_fmac_f32_e32 v70, v50, v64
	v_fmac_f32_e32 v65, v54, v64
	v_mul_f32_e32 v64, v53, v67
	v_fmac_f32_e32 v64, v52, v66
	v_mul_f32_e32 v71, v49, v67
	v_add_f32_e32 v64, v65, v64
	v_fmac_f32_e32 v71, v48, v66
	v_add_f32_e32 v69, v69, v64
	ds_read_b128 v[64:67], v93 offset:10240
	v_add_f32_e32 v70, v70, v71
	v_add_f32_e32 v68, v68, v70
	ds_swizzle_b32 v11, v10 offset:swizzle(SWAP,4)
	s_waitcnt lgkmcnt(2)
	v_add_f32_e32 v8, v8, v9
	s_waitcnt lgkmcnt(1)
	v_mul_f32_e32 v70, v59, v65
	v_mul_f32_e32 v65, v43, v65
	v_fmac_f32_e32 v70, v58, v64
	v_fmac_f32_e32 v65, v42, v64
	v_mul_f32_e32 v64, v41, v67
	v_fmac_f32_e32 v64, v40, v66
	v_mul_f32_e32 v71, v57, v67
	v_add_f32_e32 v64, v65, v64
	v_fmac_f32_e32 v71, v56, v66
	v_add_f32_e32 v69, v69, v64
	ds_read_b128 v[64:67], v93 offset:11264
	v_add_f32_e32 v70, v70, v71
	v_add_f32_e32 v68, v68, v70
	s_waitcnt lgkmcnt(1)
	v_add_f32_e32 v10, v10, v11
	ds_swizzle_b32 v9, v8 offset:swizzle(SWAP,8)
	s_waitcnt lgkmcnt(1)
	v_mul_f32_e32 v70, v31, v65
	v_mul_f32_e32 v65, v35, v65
	v_fmac_f32_e32 v70, v30, v64
	v_fmac_f32_e32 v65, v34, v64
	v_mul_f32_e32 v64, v33, v67
	v_fmac_f32_e32 v64, v32, v66
	v_mul_f32_e32 v71, v29, v67
	v_add_f32_e32 v64, v65, v64
	v_fmac_f32_e32 v71, v28, v66
	v_add_f32_e32 v69, v69, v64
	ds_read_b128 v[64:67], v93 offset:12288
	v_add_f32_e32 v70, v70, v71
	v_add_f32_e32 v68, v68, v70
	ds_swizzle_b32 v11, v10 offset:swizzle(SWAP,8)
	s_waitcnt lgkmcnt(2)
	v_add_f32_e32 v8, v8, v9
	s_waitcnt lgkmcnt(1)
	v_mul_f32_e32 v70, v47, v65
	v_mul_f32_e32 v65, v27, v65
	v_fmac_f32_e32 v70, v46, v64
	v_fmac_f32_e32 v65, v26, v64
	v_mul_f32_e32 v64, v25, v67
	v_fmac_f32_e32 v64, v24, v66
	v_mul_f32_e32 v71, v45, v67
	v_add_f32_e32 v64, v65, v64
	v_fmac_f32_e32 v71, v44, v66
	v_add_f32_e32 v69, v69, v64
	ds_read_b128 v[64:67], v93 offset:13312
	v_add_f32_e32 v70, v70, v71
	v_add_f32_e32 v68, v68, v70
	s_waitcnt lgkmcnt(1)
	v_add_f32_e32 v10, v10, v11
	ds_swizzle_b32 v9, v8 offset:swizzle(SWAP,16)
	s_waitcnt lgkmcnt(1)
	v_mul_f32_e32 v70, v19, v65
	v_mul_f32_e32 v65, v23, v65
	v_fmac_f32_e32 v70, v18, v64
	v_fmac_f32_e32 v65, v22, v64
	v_mul_f32_e32 v64, v21, v67
	v_fmac_f32_e32 v64, v20, v66
	v_mul_f32_e32 v71, v17, v67
	v_add_f32_e32 v64, v65, v64
	v_fmac_f32_e32 v71, v16, v66
	v_add_f32_e32 v69, v69, v64
	ds_read_b128 v[64:67], v93 offset:14336
	v_add_f32_e32 v70, v70, v71
	v_add_f32_e32 v68, v68, v70
	ds_swizzle_b32 v11, v10 offset:swizzle(SWAP,16)
	s_waitcnt lgkmcnt(2)
	v_add_f32_e32 v8, v8, v9
	s_waitcnt lgkmcnt(1)
	v_mul_f32_e32 v70, v39, v65
	v_mul_f32_e32 v65, v15, v65
	v_fmac_f32_e32 v70, v38, v64
	v_fmac_f32_e32 v65, v14, v64
	v_mul_f32_e32 v64, v13, v67
	v_fmac_f32_e32 v64, v12, v66
	v_mul_f32_e32 v71, v37, v67
	v_add_f32_e32 v64, v65, v64
	v_fmac_f32_e32 v71, v36, v66
	v_add_f32_e32 v69, v69, v64
	ds_read_b128 v[64:67], v93 offset:15360
	v_add_f32_e32 v70, v70, v71
	v_add_f32_e32 v68, v68, v70
	s_waitcnt lgkmcnt(1)
	v_add_f32_e32 v10, v10, v11
	v_mov_b32_e32 v9, v8
	s_waitcnt lgkmcnt(0)
	v_mul_f32_e32 v70, v5, v65
	v_mul_f32_e32 v71, v1, v67
	v_mul_f32_e32 v65, v7, v65
	v_fmac_f32_e32 v70, v4, v64
	v_fmac_f32_e32 v71, v0, v66
	v_fmac_f32_e32 v65, v6, v64
	v_mul_f32_e32 v64, v3, v67
	v_add_f32_e32 v70, v70, v71
	v_fmac_f32_e32 v64, v2, v66
	v_add_f32_e32 v68, v68, v70
	v_add_f32_e32 v64, v65, v64
	v_add_f32_e32 v66, v69, v64
	ds_swizzle_b32 v64, v68 offset:swizzle(SWAP,1)
	ds_swizzle_b32 v67, v66 offset:swizzle(SWAP,1)
	v_mov_b32_e32 v11, v10
	v_permlane32_swap_b32_e32 v8, v9
	s_waitcnt lgkmcnt(1)
	v_add_f32_e32 v64, v68, v64
	ds_read_b128 v[68:71], v93 offset:16384
	s_waitcnt lgkmcnt(1)
	v_add_f32_e32 v66, v66, v67
	ds_swizzle_b32 v65, v64 offset:swizzle(SWAP,2)
	ds_swizzle_b32 v67, v66 offset:swizzle(SWAP,2)
	v_permlane32_swap_b32_e32 v10, v11
	s_waitcnt lgkmcnt(2)
	v_mul_f32_e32 v85, v89, v69
	v_mul_f32_e32 v69, v63, v69
	v_fmac_f32_e32 v85, v88, v68
	v_fmac_f32_e32 v69, v62, v68
	v_mul_f32_e32 v68, v61, v71
	v_mul_f32_e32 v90, v87, v71
	v_fmac_f32_e32 v68, v60, v70
	v_fmac_f32_e32 v90, v86, v70
	v_add_f32_e32 v68, v69, v68
	v_add_f32_e32 v85, v85, v90
	v_add_f32_e32 v90, 0, v68
	ds_read_b128 v[68:71], v93 offset:17408
	v_add_f32_e32 v85, 0, v85
	s_waitcnt lgkmcnt(2)
	v_add_f32_e32 v64, v64, v65
	s_waitcnt lgkmcnt(1)
	v_add_f32_e32 v66, v66, v67
	ds_swizzle_b32 v65, v64 offset:swizzle(SWAP,4)
	s_waitcnt lgkmcnt(1)
	v_mul_f32_e32 v91, v51, v69
	v_mul_f32_e32 v69, v55, v69
	v_fmac_f32_e32 v91, v50, v68
	v_fmac_f32_e32 v69, v54, v68
	v_mul_f32_e32 v68, v53, v71
	v_fmac_f32_e32 v68, v52, v70
	v_mul_f32_e32 v92, v49, v71
	v_add_f32_e32 v68, v69, v68
	v_fmac_f32_e32 v92, v48, v70
	v_add_f32_e32 v90, v90, v68
	ds_read_b128 v[68:71], v93 offset:18432
	v_add_f32_e32 v91, v91, v92
	v_add_f32_e32 v85, v85, v91
	ds_swizzle_b32 v67, v66 offset:swizzle(SWAP,4)
	s_waitcnt lgkmcnt(2)
	v_add_f32_e32 v64, v64, v65
	s_waitcnt lgkmcnt(1)
	v_mul_f32_e32 v91, v59, v69
	v_mul_f32_e32 v69, v43, v69
	v_fmac_f32_e32 v91, v58, v68
	v_fmac_f32_e32 v69, v42, v68
	v_mul_f32_e32 v68, v41, v71
	v_fmac_f32_e32 v68, v40, v70
	v_mul_f32_e32 v92, v57, v71
	v_add_f32_e32 v68, v69, v68
	v_fmac_f32_e32 v92, v56, v70
	v_add_f32_e32 v90, v90, v68
	ds_read_b128 v[68:71], v93 offset:19456
	v_add_f32_e32 v91, v91, v92
	v_add_f32_e32 v85, v85, v91
	s_waitcnt lgkmcnt(1)
	v_add_f32_e32 v66, v66, v67
	ds_swizzle_b32 v65, v64 offset:swizzle(SWAP,8)
	s_waitcnt lgkmcnt(1)
	v_mul_f32_e32 v91, v31, v69
	v_mul_f32_e32 v69, v35, v69
	v_fmac_f32_e32 v91, v30, v68
	v_fmac_f32_e32 v69, v34, v68
	v_mul_f32_e32 v68, v33, v71
	v_fmac_f32_e32 v68, v32, v70
	v_mul_f32_e32 v92, v29, v71
	v_add_f32_e32 v68, v69, v68
	v_fmac_f32_e32 v92, v28, v70
	v_add_f32_e32 v90, v90, v68
	ds_read_b128 v[68:71], v93 offset:20480
	v_add_f32_e32 v91, v91, v92
	v_add_f32_e32 v85, v85, v91
	ds_swizzle_b32 v67, v66 offset:swizzle(SWAP,8)
	s_waitcnt lgkmcnt(2)
	v_add_f32_e32 v64, v64, v65
	s_waitcnt lgkmcnt(1)
	v_mul_f32_e32 v91, v47, v69
	v_mul_f32_e32 v69, v27, v69
	v_fmac_f32_e32 v91, v46, v68
	v_fmac_f32_e32 v69, v26, v68
	v_mul_f32_e32 v68, v25, v71
	v_fmac_f32_e32 v68, v24, v70
	v_mul_f32_e32 v92, v45, v71
	v_add_f32_e32 v68, v69, v68
	v_fmac_f32_e32 v92, v44, v70
	v_add_f32_e32 v90, v90, v68
	ds_read_b128 v[68:71], v93 offset:21504
	v_add_f32_e32 v91, v91, v92
	v_add_f32_e32 v85, v85, v91
	s_waitcnt lgkmcnt(1)
	v_add_f32_e32 v66, v66, v67
	ds_swizzle_b32 v65, v64 offset:swizzle(SWAP,16)
	s_waitcnt lgkmcnt(1)
	v_mul_f32_e32 v91, v19, v69
	v_mul_f32_e32 v69, v23, v69
	v_fmac_f32_e32 v91, v18, v68
	v_fmac_f32_e32 v69, v22, v68
	v_mul_f32_e32 v68, v21, v71
	v_fmac_f32_e32 v68, v20, v70
	v_mul_f32_e32 v92, v17, v71
	v_add_f32_e32 v68, v69, v68
	v_fmac_f32_e32 v92, v16, v70
	v_add_f32_e32 v90, v90, v68
	ds_read_b128 v[68:71], v93 offset:22528
	v_add_f32_e32 v91, v91, v92
	v_add_f32_e32 v85, v85, v91
	ds_swizzle_b32 v67, v66 offset:swizzle(SWAP,16)
	s_waitcnt lgkmcnt(2)
	v_add_f32_e32 v64, v64, v65
	s_waitcnt lgkmcnt(1)
	v_mul_f32_e32 v91, v39, v69
	v_mul_f32_e32 v69, v15, v69
	v_fmac_f32_e32 v91, v38, v68
	v_fmac_f32_e32 v69, v14, v68
	v_mul_f32_e32 v68, v13, v71
	v_fmac_f32_e32 v68, v12, v70
	v_mul_f32_e32 v92, v37, v71
	v_add_f32_e32 v68, v69, v68
	v_fmac_f32_e32 v92, v36, v70
	v_add_f32_e32 v90, v90, v68
	ds_read_b128 v[68:71], v93 offset:23552
	v_add_f32_e32 v91, v91, v92
	v_add_f32_e32 v85, v85, v91
	s_waitcnt lgkmcnt(1)
	v_add_f32_e32 v66, v66, v67
	v_mov_b32_e32 v65, v64
	s_waitcnt lgkmcnt(0)
	v_mul_f32_e32 v91, v5, v69
	v_mul_f32_e32 v92, v1, v71
	v_mul_f32_e32 v69, v7, v69
	v_fmac_f32_e32 v91, v4, v68
	v_fmac_f32_e32 v92, v0, v70
	v_fmac_f32_e32 v69, v6, v68
	v_mul_f32_e32 v68, v3, v71
	v_add_f32_e32 v91, v91, v92
	v_fmac_f32_e32 v68, v2, v70
	v_add_f32_e32 v85, v85, v91
	v_add_f32_e32 v68, v69, v68
	v_add_f32_e32 v70, v90, v68
	ds_swizzle_b32 v68, v85 offset:swizzle(SWAP,1)
	v_mul_f32_e32 v90, v87, v97
	v_fmac_f32_e32 v90, v86, v96
	v_mul_f32_e32 v91, v61, v97
	v_fmac_f32_e32 v91, v60, v96
	s_waitcnt lgkmcnt(0)
	v_add_f32_e32 v68, v85, v68
	v_mul_f32_e32 v85, v89, v95
	v_fmac_f32_e32 v85, v88, v94
	v_add_f32_e32 v85, v85, v90
	v_mul_f32_e32 v90, v63, v95
	v_fmac_f32_e32 v90, v62, v94
	ds_read_b128 v[94:97], v93 offset:25600
	v_add_f32_e32 v90, v90, v91
	v_add_f32_e32 v85, 0, v85
	v_add_f32_e32 v90, 0, v90
	ds_swizzle_b32 v71, v70 offset:swizzle(SWAP,1)
	s_waitcnt lgkmcnt(1)
	v_mul_f32_e32 v91, v51, v95
	v_mul_f32_e32 v92, v49, v97
	v_fmac_f32_e32 v91, v50, v94
	v_fmac_f32_e32 v92, v48, v96
	v_add_f32_e32 v91, v91, v92
	v_add_f32_e32 v85, v85, v91
	v_mul_f32_e32 v91, v55, v95
	v_mul_f32_e32 v92, v53, v97
	v_fmac_f32_e32 v91, v54, v94
	v_fmac_f32_e32 v92, v52, v96
	ds_read_b128 v[94:97], v93 offset:26624
	v_add_f32_e32 v91, v91, v92
	v_add_f32_e32 v90, v90, v91
	s_waitcnt lgkmcnt(1)
	v_add_f32_e32 v70, v70, v71
	ds_swizzle_b32 v69, v68 offset:swizzle(SWAP,2)
	s_waitcnt lgkmcnt(1)
	v_mul_f32_e32 v91, v59, v95
	v_mul_f32_e32 v92, v57, v97
	v_fmac_f32_e32 v91, v58, v94
	v_fmac_f32_e32 v92, v56, v96
	v_add_f32_e32 v91, v91, v92
	v_add_f32_e32 v85, v85, v91
	v_mul_f32_e32 v91, v43, v95
	v_mul_f32_e32 v92, v41, v97
	v_fmac_f32_e32 v91, v42, v94
	v_fmac_f32_e32 v92, v40, v96
	ds_read_b128 v[94:97], v93 offset:27648
	v_add_f32_e32 v91, v91, v92
	v_add_f32_e32 v90, v90, v91
	ds_swizzle_b32 v71, v70 offset:swizzle(SWAP,2)
	s_waitcnt lgkmcnt(2)
	v_add_f32_e32 v68, v68, v69
	s_waitcnt lgkmcnt(1)
	v_mul_f32_e32 v91, v31, v95
	v_mul_f32_e32 v92, v29, v97
	v_fmac_f32_e32 v91, v30, v94
	v_fmac_f32_e32 v92, v28, v96
	v_add_f32_e32 v91, v91, v92
	v_add_f32_e32 v85, v85, v91
	v_mul_f32_e32 v91, v35, v95
	v_mul_f32_e32 v92, v33, v97
	v_fmac_f32_e32 v91, v34, v94
	v_fmac_f32_e32 v92, v32, v96
	ds_read_b128 v[94:97], v93 offset:28672
	v_add_f32_e32 v91, v91, v92
	v_add_f32_e32 v90, v90, v91
	s_waitcnt lgkmcnt(1)
	v_add_f32_e32 v70, v70, v71
	ds_swizzle_b32 v69, v68 offset:swizzle(SWAP,4)
	s_waitcnt lgkmcnt(1)
	v_mul_f32_e32 v91, v47, v95
	v_mul_f32_e32 v92, v45, v97
	v_fmac_f32_e32 v91, v46, v94
	v_fmac_f32_e32 v92, v44, v96
	v_add_f32_e32 v91, v91, v92
	v_add_f32_e32 v85, v85, v91
	v_mul_f32_e32 v91, v27, v95
	v_mul_f32_e32 v92, v25, v97
	v_fmac_f32_e32 v91, v26, v94
	v_fmac_f32_e32 v92, v24, v96
	ds_read_b128 v[94:97], v93 offset:29696
	v_add_f32_e32 v91, v91, v92
	v_add_f32_e32 v90, v90, v91
	ds_swizzle_b32 v71, v70 offset:swizzle(SWAP,4)
	s_waitcnt lgkmcnt(2)
	v_add_f32_e32 v68, v68, v69
	s_waitcnt lgkmcnt(1)
	v_mul_f32_e32 v91, v19, v95
	v_mul_f32_e32 v92, v17, v97
	v_fmac_f32_e32 v91, v18, v94
	v_fmac_f32_e32 v92, v16, v96
	v_add_f32_e32 v91, v91, v92
	v_add_f32_e32 v85, v85, v91
	v_mul_f32_e32 v91, v23, v95
	v_mul_f32_e32 v92, v21, v97
	v_fmac_f32_e32 v91, v22, v94
	v_fmac_f32_e32 v92, v20, v96
	ds_read_b128 v[94:97], v93 offset:30720
	v_add_f32_e32 v91, v91, v92
	v_add_f32_e32 v90, v90, v91
	s_waitcnt lgkmcnt(1)
	v_add_f32_e32 v70, v70, v71
	ds_swizzle_b32 v69, v68 offset:swizzle(SWAP,8)
	s_waitcnt lgkmcnt(1)
	v_mul_f32_e32 v91, v39, v95
	v_mul_f32_e32 v92, v37, v97
	v_fmac_f32_e32 v91, v38, v94
	v_fmac_f32_e32 v92, v36, v96
	v_add_f32_e32 v91, v91, v92
	v_add_f32_e32 v85, v85, v91
	v_mul_f32_e32 v91, v15, v95
	v_mul_f32_e32 v92, v13, v97
	v_fmac_f32_e32 v91, v14, v94
	v_fmac_f32_e32 v92, v12, v96
	ds_read_b128 v[94:97], v93 offset:31744
	v_add_f32_e32 v91, v91, v92
	v_add_f32_e32 v90, v90, v91
	ds_swizzle_b32 v71, v70 offset:swizzle(SWAP,8)
	s_waitcnt lgkmcnt(2)
	v_add_f32_e32 v68, v68, v69
	s_waitcnt lgkmcnt(1)
	v_mul_f32_e32 v91, v5, v95
	v_mul_f32_e32 v92, v1, v97
	v_fmac_f32_e32 v91, v4, v94
	v_fmac_f32_e32 v92, v0, v96
	v_add_f32_e32 v91, v91, v92
	v_add_f32_e32 v85, v85, v91
	v_mul_f32_e32 v91, v7, v95
	v_mul_f32_e32 v92, v3, v97
	v_fmac_f32_e32 v91, v6, v94
	v_fmac_f32_e32 v92, v2, v96
	ds_read_b128 v[94:97], v93 offset:32768
	v_add_f32_e32 v91, v91, v92
	v_add_f32_e32 v91, v90, v91
	ds_swizzle_b32 v90, v85 offset:swizzle(SWAP,1)
	ds_swizzle_b32 v92, v91 offset:swizzle(SWAP,1)
	s_waitcnt lgkmcnt(2)
	v_mul_f32_e32 v98, v89, v95
	v_mul_f32_e32 v95, v63, v95
	v_fmac_f32_e32 v98, v88, v94
	v_fmac_f32_e32 v95, v62, v94
	v_mul_f32_e32 v94, v61, v97
	v_mul_f32_e32 v99, v87, v97
	v_fmac_f32_e32 v94, v60, v96
	v_fmac_f32_e32 v99, v86, v96
	v_add_f32_e32 v94, v95, v94
	v_add_f32_e32 v98, v98, v99
	v_add_f32_e32 v99, 0, v94
	ds_read_b128 v[94:97], v93 offset:33792
	v_add_f32_e32 v98, 0, v98
	s_waitcnt lgkmcnt(2)
	v_add_f32_e32 v85, v85, v90
	s_waitcnt lgkmcnt(1)
	v_add_f32_e32 v91, v91, v92
	ds_swizzle_b32 v90, v85 offset:swizzle(SWAP,2)
	s_waitcnt lgkmcnt(1)
	v_mul_f32_e32 v100, v51, v95
	v_mul_f32_e32 v95, v55, v95
	v_fmac_f32_e32 v100, v50, v94
	v_fmac_f32_e32 v95, v54, v94
	v_mul_f32_e32 v94, v53, v97
	v_fmac_f32_e32 v94, v52, v96
	v_mul_f32_e32 v101, v49, v97
	v_add_f32_e32 v94, v95, v94
	v_fmac_f32_e32 v101, v48, v96
	v_add_f32_e32 v99, v99, v94
	ds_read_b128 v[94:97], v93 offset:34816
	v_add_f32_e32 v100, v100, v101
	v_add_f32_e32 v98, v98, v100
	ds_swizzle_b32 v92, v91 offset:swizzle(SWAP,2)
	s_waitcnt lgkmcnt(2)
	v_add_f32_e32 v85, v85, v90
	s_waitcnt lgkmcnt(1)
	v_mul_f32_e32 v100, v59, v95
	v_mul_f32_e32 v95, v43, v95
	v_fmac_f32_e32 v100, v58, v94
	v_fmac_f32_e32 v95, v42, v94
	v_mul_f32_e32 v94, v41, v97
	v_fmac_f32_e32 v94, v40, v96
	v_mul_f32_e32 v101, v57, v97
	v_add_f32_e32 v94, v95, v94
	v_fmac_f32_e32 v101, v56, v96
	v_add_f32_e32 v99, v99, v94
	ds_read_b128 v[94:97], v93 offset:35840
	v_add_f32_e32 v100, v100, v101
	v_add_f32_e32 v98, v98, v100
	s_waitcnt lgkmcnt(1)
	v_add_f32_e32 v91, v91, v92
	ds_swizzle_b32 v90, v85 offset:swizzle(SWAP,4)
	s_waitcnt lgkmcnt(1)
	v_mul_f32_e32 v100, v31, v95
	v_mul_f32_e32 v95, v35, v95
	v_fmac_f32_e32 v100, v30, v94
	v_fmac_f32_e32 v95, v34, v94
	v_mul_f32_e32 v94, v33, v97
	v_fmac_f32_e32 v94, v32, v96
	v_mul_f32_e32 v101, v29, v97
	v_add_f32_e32 v94, v95, v94
	v_fmac_f32_e32 v101, v28, v96
	v_add_f32_e32 v99, v99, v94
	ds_read_b128 v[94:97], v93 offset:36864
	v_add_f32_e32 v100, v100, v101
	v_add_f32_e32 v98, v98, v100
	ds_swizzle_b32 v92, v91 offset:swizzle(SWAP,4)
	s_waitcnt lgkmcnt(2)
	v_add_f32_e32 v85, v85, v90
	s_waitcnt lgkmcnt(1)
	v_mul_f32_e32 v100, v47, v95
	v_mul_f32_e32 v95, v27, v95
	v_fmac_f32_e32 v100, v46, v94
	v_fmac_f32_e32 v95, v26, v94
	v_mul_f32_e32 v94, v25, v97
	v_fmac_f32_e32 v94, v24, v96
	v_mul_f32_e32 v101, v45, v97
	v_add_f32_e32 v94, v95, v94
	v_fmac_f32_e32 v101, v44, v96
	v_add_f32_e32 v99, v99, v94
	ds_read_b128 v[94:97], v93 offset:37888
	v_add_f32_e32 v100, v100, v101
	v_add_f32_e32 v98, v98, v100
	s_waitcnt lgkmcnt(1)
	v_add_f32_e32 v91, v91, v92
	ds_swizzle_b32 v90, v85 offset:swizzle(SWAP,8)
	s_waitcnt lgkmcnt(1)
	v_mul_f32_e32 v100, v19, v95
	v_mul_f32_e32 v95, v23, v95
	v_fmac_f32_e32 v100, v18, v94
	v_fmac_f32_e32 v95, v22, v94
	v_mul_f32_e32 v94, v21, v97
	v_fmac_f32_e32 v94, v20, v96
	v_mul_f32_e32 v101, v17, v97
	v_add_f32_e32 v94, v95, v94
	v_fmac_f32_e32 v101, v16, v96
	v_add_f32_e32 v99, v99, v94
	ds_read_b128 v[94:97], v93 offset:38912
	v_add_f32_e32 v100, v100, v101
	v_add_f32_e32 v98, v98, v100
	ds_swizzle_b32 v92, v91 offset:swizzle(SWAP,8)
	v_add_f32_e32 v70, v70, v71
	s_waitcnt lgkmcnt(1)
	v_mul_f32_e32 v100, v39, v95
	v_mul_f32_e32 v95, v15, v95
	v_fmac_f32_e32 v100, v38, v94
	v_fmac_f32_e32 v95, v14, v94
	v_mul_f32_e32 v94, v13, v97
	v_fmac_f32_e32 v94, v12, v96
	v_mul_f32_e32 v101, v37, v97
	v_add_f32_e32 v94, v95, v94
	v_fmac_f32_e32 v101, v36, v96
	v_add_f32_e32 v99, v99, v94
	ds_read_b128 v[94:97], v93 offset:39936
	v_add_f32_e32 v100, v100, v101
	v_add_f32_e32 v98, v98, v100
	v_add_f32_e32 v85, v85, v90
	s_waitcnt lgkmcnt(1)
	v_add_f32_e32 v91, v91, v92
	s_waitcnt lgkmcnt(0)
	v_mul_f32_e32 v100, v5, v95
	v_mul_f32_e32 v101, v1, v97
	v_mul_f32_e32 v95, v7, v95
	v_fmac_f32_e32 v100, v4, v94
	v_fmac_f32_e32 v101, v0, v96
	v_fmac_f32_e32 v95, v6, v94
	v_mul_f32_e32 v94, v3, v97
	v_add_f32_e32 v100, v100, v101
	v_fmac_f32_e32 v94, v2, v96
	v_add_f32_e32 v98, v98, v100
	v_add_f32_e32 v94, v95, v94
	v_add_f32_e32 v96, v99, v94
	ds_swizzle_b32 v94, v98 offset:swizzle(SWAP,1)
	ds_swizzle_b32 v97, v96 offset:swizzle(SWAP,1)
	ds_swizzle_b32 v69, v68 offset:swizzle(SWAP,16)
	ds_swizzle_b32 v71, v70 offset:swizzle(SWAP,16)
	ds_swizzle_b32 v90, v85 offset:swizzle(SWAP,16)
	s_waitcnt lgkmcnt(4)
	v_add_f32_e32 v94, v98, v94
	ds_read_b128 v[98:101], v93 offset:40960
	s_waitcnt lgkmcnt(4)
	v_add_f32_e32 v96, v96, v97
	ds_swizzle_b32 v95, v94 offset:swizzle(SWAP,2)
	ds_swizzle_b32 v97, v96 offset:swizzle(SWAP,2)
	ds_swizzle_b32 v92, v91 offset:swizzle(SWAP,16)
	s_waitcnt lgkmcnt(3)
	v_mul_f32_e32 v102, v89, v99
	v_mul_f32_e32 v99, v63, v99
	v_fmac_f32_e32 v102, v88, v98
	v_fmac_f32_e32 v99, v62, v98
	v_mul_f32_e32 v98, v61, v101
	v_mul_f32_e32 v103, v87, v101
	v_fmac_f32_e32 v98, v60, v100
	v_fmac_f32_e32 v103, v86, v100
	v_add_f32_e32 v98, v99, v98
	v_add_f32_e32 v102, v102, v103
	v_add_f32_e32 v103, 0, v98
	ds_read_b128 v[98:101], v93 offset:41984
	v_add_f32_e32 v102, 0, v102
	s_waitcnt lgkmcnt(3)
	v_add_f32_e32 v94, v94, v95
	s_waitcnt lgkmcnt(2)
	v_add_f32_e32 v96, v96, v97
	ds_swizzle_b32 v95, v94 offset:swizzle(SWAP,4)
	s_waitcnt lgkmcnt(1)
	v_mul_f32_e32 v104, v51, v99
	v_mul_f32_e32 v99, v55, v99
	v_fmac_f32_e32 v104, v50, v98
	v_fmac_f32_e32 v99, v54, v98
	v_mul_f32_e32 v98, v53, v101
	v_fmac_f32_e32 v98, v52, v100
	v_mul_f32_e32 v105, v49, v101
	v_add_f32_e32 v98, v99, v98
	v_fmac_f32_e32 v105, v48, v100
	v_add_f32_e32 v103, v103, v98
	ds_read_b128 v[98:101], v93 offset:43008
	v_add_f32_e32 v104, v104, v105
	v_add_f32_e32 v102, v102, v104
	ds_swizzle_b32 v97, v96 offset:swizzle(SWAP,4)
	s_waitcnt lgkmcnt(2)
	v_add_f32_e32 v94, v94, v95
	s_waitcnt lgkmcnt(1)
	v_mul_f32_e32 v104, v59, v99
	v_mul_f32_e32 v99, v43, v99
	v_fmac_f32_e32 v104, v58, v98
	v_fmac_f32_e32 v99, v42, v98
	v_mul_f32_e32 v98, v41, v101
	v_fmac_f32_e32 v98, v40, v100
	v_mul_f32_e32 v105, v57, v101
	v_add_f32_e32 v98, v99, v98
	v_fmac_f32_e32 v105, v56, v100
	v_add_f32_e32 v103, v103, v98
	ds_read_b128 v[98:101], v93 offset:44032
	v_add_f32_e32 v104, v104, v105
	v_add_f32_e32 v102, v102, v104
	s_waitcnt lgkmcnt(1)
	v_add_f32_e32 v96, v96, v97
	ds_swizzle_b32 v95, v94 offset:swizzle(SWAP,8)
	s_waitcnt lgkmcnt(1)
	v_mul_f32_e32 v104, v31, v99
	v_mul_f32_e32 v99, v35, v99
	v_fmac_f32_e32 v104, v30, v98
	v_fmac_f32_e32 v99, v34, v98
	v_mul_f32_e32 v98, v33, v101
	v_fmac_f32_e32 v98, v32, v100
	v_mul_f32_e32 v105, v29, v101
	v_add_f32_e32 v98, v99, v98
	v_fmac_f32_e32 v105, v28, v100
	v_add_f32_e32 v103, v103, v98
	ds_read_b128 v[98:101], v93 offset:45056
	v_add_f32_e32 v104, v104, v105
	v_add_f32_e32 v102, v102, v104
	ds_swizzle_b32 v97, v96 offset:swizzle(SWAP,8)
	s_waitcnt lgkmcnt(2)
	v_add_f32_e32 v94, v94, v95
	s_waitcnt lgkmcnt(1)
	v_mul_f32_e32 v104, v47, v99
	v_mul_f32_e32 v99, v27, v99
	v_fmac_f32_e32 v104, v46, v98
	v_fmac_f32_e32 v99, v26, v98
	v_mul_f32_e32 v98, v25, v101
	v_fmac_f32_e32 v98, v24, v100
	v_mul_f32_e32 v105, v45, v101
	v_add_f32_e32 v98, v99, v98
	v_fmac_f32_e32 v105, v44, v100
	v_add_f32_e32 v103, v103, v98
	ds_read_b128 v[98:101], v93 offset:46080
	v_add_f32_e32 v104, v104, v105
	v_add_f32_e32 v102, v102, v104
	s_waitcnt lgkmcnt(1)
	v_add_f32_e32 v96, v96, v97
	ds_swizzle_b32 v95, v94 offset:swizzle(SWAP,16)
	s_waitcnt lgkmcnt(1)
	v_mul_f32_e32 v104, v19, v99
	v_mul_f32_e32 v99, v23, v99
	v_fmac_f32_e32 v104, v18, v98
	v_fmac_f32_e32 v99, v22, v98
	v_mul_f32_e32 v98, v21, v101
	v_fmac_f32_e32 v98, v20, v100
	v_mul_f32_e32 v105, v17, v101
	v_add_f32_e32 v98, v99, v98
	v_fmac_f32_e32 v105, v16, v100
	v_add_f32_e32 v103, v103, v98
	ds_read_b128 v[98:101], v93 offset:47104
	v_add_f32_e32 v104, v104, v105
	v_add_f32_e32 v102, v102, v104
	ds_swizzle_b32 v97, v96 offset:swizzle(SWAP,16)
	v_add_f32_e32 v68, v68, v69
	s_waitcnt lgkmcnt(1)
	v_mul_f32_e32 v104, v39, v99
	v_mul_f32_e32 v99, v15, v99
	v_fmac_f32_e32 v104, v38, v98
	v_fmac_f32_e32 v99, v14, v98
	v_mul_f32_e32 v98, v13, v101
	v_fmac_f32_e32 v98, v12, v100
	v_mul_f32_e32 v105, v37, v101
	v_add_f32_e32 v98, v99, v98
	v_fmac_f32_e32 v105, v36, v100
	v_add_f32_e32 v103, v103, v98
	ds_read_b128 v[98:101], v93 offset:48128
	v_add_f32_e32 v104, v104, v105
	v_add_f32_e32 v102, v102, v104
	v_add_f32_e32 v70, v70, v71
	v_add_f32_e32 v85, v85, v90
	s_waitcnt lgkmcnt(0)
	v_mul_f32_e32 v104, v5, v99
	v_mul_f32_e32 v105, v1, v101
	v_mul_f32_e32 v99, v7, v99
	v_fmac_f32_e32 v104, v4, v98
	v_fmac_f32_e32 v105, v0, v100
	v_fmac_f32_e32 v99, v6, v98
	v_mul_f32_e32 v98, v3, v101
	v_add_f32_e32 v104, v104, v105
	v_fmac_f32_e32 v98, v2, v100
	v_add_f32_e32 v102, v102, v104
	v_add_f32_e32 v98, v99, v98
	v_add_f32_e32 v100, v103, v98
	ds_swizzle_b32 v98, v102 offset:swizzle(SWAP,1)
	ds_swizzle_b32 v101, v100 offset:swizzle(SWAP,1)
	v_add_f32_e32 v91, v91, v92
	v_add_f32_e32 v94, v94, v95
	v_add_f32_e32 v96, v96, v97
	s_waitcnt lgkmcnt(1)
	v_add_f32_e32 v98, v102, v98
	ds_read_b128 v[102:105], v93 offset:49152
	s_waitcnt lgkmcnt(1)
	v_add_f32_e32 v100, v100, v101
	ds_swizzle_b32 v99, v98 offset:swizzle(SWAP,2)
	ds_swizzle_b32 v101, v100 offset:swizzle(SWAP,2)
	v_mov_b32_e32 v67, v66
	s_waitcnt lgkmcnt(2)
	v_mul_f32_e32 v106, v89, v103
	v_mul_f32_e32 v103, v63, v103
	v_fmac_f32_e32 v106, v88, v102
	v_fmac_f32_e32 v103, v62, v102
	v_mul_f32_e32 v102, v61, v105
	v_mul_f32_e32 v107, v87, v105
	v_fmac_f32_e32 v102, v60, v104
	v_fmac_f32_e32 v107, v86, v104
	v_add_f32_e32 v102, v103, v102
	v_add_f32_e32 v106, v106, v107
	v_add_f32_e32 v107, 0, v102
	ds_read_b128 v[102:105], v93 offset:50176
	v_add_f32_e32 v106, 0, v106
	s_waitcnt lgkmcnt(2)
	v_add_f32_e32 v98, v98, v99
	s_waitcnt lgkmcnt(1)
	v_add_f32_e32 v100, v100, v101
	ds_swizzle_b32 v99, v98 offset:swizzle(SWAP,4)
	s_waitcnt lgkmcnt(1)
	v_mul_f32_e32 v108, v51, v103
	v_mul_f32_e32 v103, v55, v103
	v_fmac_f32_e32 v108, v50, v102
	v_fmac_f32_e32 v103, v54, v102
	v_mul_f32_e32 v102, v53, v105
	v_fmac_f32_e32 v102, v52, v104
	v_mul_f32_e32 v109, v49, v105
	v_add_f32_e32 v102, v103, v102
	v_fmac_f32_e32 v109, v48, v104
	v_add_f32_e32 v107, v107, v102
	ds_read_b128 v[102:105], v93 offset:51200
	v_add_f32_e32 v108, v108, v109
	v_add_f32_e32 v106, v106, v108
	ds_swizzle_b32 v101, v100 offset:swizzle(SWAP,4)
	s_waitcnt lgkmcnt(2)
	v_add_f32_e32 v98, v98, v99
	s_waitcnt lgkmcnt(1)
	v_mul_f32_e32 v108, v59, v103
	v_mul_f32_e32 v103, v43, v103
	v_fmac_f32_e32 v108, v58, v102
	v_fmac_f32_e32 v103, v42, v102
	v_mul_f32_e32 v102, v41, v105
	v_fmac_f32_e32 v102, v40, v104
	v_mul_f32_e32 v109, v57, v105
	v_add_f32_e32 v102, v103, v102
	v_fmac_f32_e32 v109, v56, v104
	v_add_f32_e32 v107, v107, v102
	ds_read_b128 v[102:105], v93 offset:52224
	v_add_f32_e32 v108, v108, v109
	v_add_f32_e32 v106, v106, v108
	s_waitcnt lgkmcnt(1)
	v_add_f32_e32 v100, v100, v101
	ds_swizzle_b32 v99, v98 offset:swizzle(SWAP,8)
	s_waitcnt lgkmcnt(1)
	v_mul_f32_e32 v108, v31, v103
	v_mul_f32_e32 v103, v35, v103
	v_fmac_f32_e32 v108, v30, v102
	v_fmac_f32_e32 v103, v34, v102
	v_mul_f32_e32 v102, v33, v105
	v_fmac_f32_e32 v102, v32, v104
	v_mul_f32_e32 v109, v29, v105
	v_add_f32_e32 v102, v103, v102
	v_fmac_f32_e32 v109, v28, v104
	v_add_f32_e32 v107, v107, v102
	ds_read_b128 v[102:105], v93 offset:53248
	v_add_f32_e32 v108, v108, v109
	v_add_f32_e32 v106, v106, v108
	ds_swizzle_b32 v101, v100 offset:swizzle(SWAP,8)
	s_waitcnt lgkmcnt(2)
	v_add_f32_e32 v98, v98, v99
	s_waitcnt lgkmcnt(1)
	v_mul_f32_e32 v108, v47, v103
	v_mul_f32_e32 v103, v27, v103
	v_fmac_f32_e32 v108, v46, v102
	v_fmac_f32_e32 v103, v26, v102
	v_mul_f32_e32 v102, v25, v105
	v_fmac_f32_e32 v102, v24, v104
	v_mul_f32_e32 v109, v45, v105
	v_add_f32_e32 v102, v103, v102
	v_fmac_f32_e32 v109, v44, v104
	v_add_f32_e32 v107, v107, v102
	ds_read_b128 v[102:105], v93 offset:54272
	v_add_f32_e32 v108, v108, v109
	v_add_f32_e32 v106, v106, v108
	s_waitcnt lgkmcnt(1)
	v_add_f32_e32 v100, v100, v101
	ds_swizzle_b32 v99, v98 offset:swizzle(SWAP,16)
	s_waitcnt lgkmcnt(1)
	v_mul_f32_e32 v108, v19, v103
	v_mul_f32_e32 v103, v23, v103
	v_fmac_f32_e32 v108, v18, v102
	v_fmac_f32_e32 v103, v22, v102
	v_mul_f32_e32 v102, v21, v105
	v_fmac_f32_e32 v102, v20, v104
	v_mul_f32_e32 v109, v17, v105
	v_add_f32_e32 v102, v103, v102
	v_fmac_f32_e32 v109, v16, v104
	v_add_f32_e32 v107, v107, v102
	ds_read_b128 v[102:105], v93 offset:55296
	v_add_f32_e32 v108, v108, v109
	v_add_f32_e32 v106, v106, v108
	ds_swizzle_b32 v101, v100 offset:swizzle(SWAP,16)
	s_waitcnt lgkmcnt(2)
	v_add_f32_e32 v98, v98, v99
	s_waitcnt lgkmcnt(1)
	v_mul_f32_e32 v108, v39, v103
	v_mul_f32_e32 v103, v15, v103
	v_fmac_f32_e32 v108, v38, v102
	v_fmac_f32_e32 v103, v14, v102
	v_mul_f32_e32 v102, v13, v105
	v_fmac_f32_e32 v102, v12, v104
	v_mul_f32_e32 v109, v37, v105
	v_add_f32_e32 v102, v103, v102
	v_fmac_f32_e32 v109, v36, v104
	v_add_f32_e32 v107, v107, v102
	ds_read_b128 v[102:105], v93 offset:56320
	v_add_f32_e32 v108, v108, v109
	v_add_f32_e32 v106, v106, v108
	s_waitcnt lgkmcnt(1)
	v_add_f32_e32 v100, v100, v101
	v_mov_b32_e32 v69, v68
	s_waitcnt lgkmcnt(0)
	v_mul_f32_e32 v108, v5, v103
	v_mul_f32_e32 v109, v1, v105
	v_mul_f32_e32 v103, v7, v103
	v_fmac_f32_e32 v108, v4, v102
	v_fmac_f32_e32 v109, v0, v104
	v_fmac_f32_e32 v103, v6, v102
	v_mul_f32_e32 v102, v3, v105
	v_add_f32_e32 v108, v108, v109
	v_fmac_f32_e32 v102, v2, v104
	v_add_f32_e32 v106, v106, v108
	v_add_f32_e32 v102, v103, v102
	v_add_f32_e32 v104, v107, v102
	ds_swizzle_b32 v102, v106 offset:swizzle(SWAP,1)
	ds_swizzle_b32 v105, v104 offset:swizzle(SWAP,1)
	v_mov_b32_e32 v71, v70
	v_mov_b32_e32 v90, v85
	v_mov_b32_e32 v92, v91
	s_waitcnt lgkmcnt(1)
	v_add_f32_e32 v102, v106, v102
	ds_read_b128 v[106:109], v93 offset:57344
	s_waitcnt lgkmcnt(1)
	v_add_f32_e32 v104, v104, v105
	ds_swizzle_b32 v103, v102 offset:swizzle(SWAP,2)
	ds_swizzle_b32 v105, v104 offset:swizzle(SWAP,2)
	v_mov_b32_e32 v95, v94
	s_waitcnt lgkmcnt(2)
	v_mul_f32_e32 v63, v63, v107
	v_mul_f32_e32 v61, v61, v109
	v_mul_f32_e32 v89, v89, v107
	v_mul_f32_e32 v87, v87, v109
	v_fmac_f32_e32 v63, v62, v106
	v_fmac_f32_e32 v61, v60, v108
	v_fmac_f32_e32 v89, v88, v106
	v_fmac_f32_e32 v87, v86, v108
	v_add_f32_e32 v60, v63, v61
	v_add_f32_e32 v86, v89, v87
	v_add_f32_e32 v87, 0, v60
	ds_read_b128 v[60:63], v93 offset:58368
	v_add_f32_e32 v86, 0, v86
	s_waitcnt lgkmcnt(2)
	v_add_f32_e32 v102, v102, v103
	s_waitcnt lgkmcnt(1)
	v_add_f32_e32 v104, v104, v105
	ds_swizzle_b32 v103, v102 offset:swizzle(SWAP,4)
	s_waitcnt lgkmcnt(1)
	v_mul_f32_e32 v51, v51, v61
	v_mul_f32_e32 v49, v49, v63
	v_fmac_f32_e32 v51, v50, v60
	v_fmac_f32_e32 v49, v48, v62
	v_add_f32_e32 v48, v51, v49
	v_add_f32_e32 v86, v86, v48
	v_mul_f32_e32 v48, v55, v61
	v_mul_f32_e32 v49, v53, v63
	v_fmac_f32_e32 v48, v54, v60
	v_fmac_f32_e32 v49, v52, v62
	v_add_f32_e32 v48, v48, v49
	v_add_f32_e32 v52, v87, v48
	ds_read_b128 v[48:51], v93 offset:59392
	ds_swizzle_b32 v105, v104 offset:swizzle(SWAP,4)
	s_waitcnt lgkmcnt(2)
	v_add_f32_e32 v102, v102, v103
	ds_swizzle_b32 v103, v102 offset:swizzle(SWAP,8)
	v_mov_b32_e32 v97, v96
	s_waitcnt lgkmcnt(2)
	v_mul_f32_e32 v43, v43, v49
	v_mul_f32_e32 v41, v41, v51
	v_fmac_f32_e32 v43, v42, v48
	v_fmac_f32_e32 v41, v40, v50
	v_mul_f32_e32 v53, v59, v49
	v_add_f32_e32 v40, v43, v41
	v_fmac_f32_e32 v53, v58, v48
	v_add_f32_e32 v48, v52, v40
	ds_read_b128 v[40:43], v93 offset:60416
	v_mul_f32_e32 v54, v57, v51
	v_fmac_f32_e32 v54, v56, v50
	v_add_f32_e32 v53, v53, v54
	v_add_f32_e32 v53, v86, v53
	s_waitcnt lgkmcnt(0)
	v_mul_f32_e32 v31, v31, v41
	v_mul_f32_e32 v29, v29, v43
	v_fmac_f32_e32 v31, v30, v40
	v_fmac_f32_e32 v29, v28, v42
	v_add_f32_e32 v28, v31, v29
	v_add_f32_e32 v49, v53, v28
	v_mul_f32_e32 v28, v35, v41
	v_mul_f32_e32 v29, v33, v43
	v_fmac_f32_e32 v28, v34, v40
	v_fmac_f32_e32 v29, v32, v42
	v_add_f32_e32 v28, v28, v29
	v_add_f32_e32 v32, v48, v28
	ds_read_b128 v[28:31], v93 offset:61440
	v_add_f32_e32 v104, v104, v105
	ds_swizzle_b32 v105, v104 offset:swizzle(SWAP,8)
	v_add_f32_e32 v102, v102, v103
	ds_swizzle_b32 v103, v102 offset:swizzle(SWAP,16)
	s_waitcnt lgkmcnt(2)
	v_mul_f32_e32 v27, v27, v29
	v_mul_f32_e32 v25, v25, v31
	v_fmac_f32_e32 v27, v26, v28
	v_fmac_f32_e32 v25, v24, v30
	v_mul_f32_e32 v33, v47, v29
	v_add_f32_e32 v24, v27, v25
	v_fmac_f32_e32 v33, v46, v28
	v_add_f32_e32 v28, v32, v24
	ds_read_b128 v[24:27], v93 offset:62464
	v_mul_f32_e32 v34, v45, v31
	v_fmac_f32_e32 v34, v44, v30
	v_add_f32_e32 v33, v33, v34
	v_add_f32_e32 v33, v49, v33
	s_waitcnt lgkmcnt(0)
	v_mul_f32_e32 v19, v19, v25
	v_mul_f32_e32 v17, v17, v27
	v_fmac_f32_e32 v19, v18, v24
	v_fmac_f32_e32 v17, v16, v26
	v_add_f32_e32 v16, v19, v17
	v_add_f32_e32 v29, v33, v16
	v_mul_f32_e32 v16, v23, v25
	v_mul_f32_e32 v17, v21, v27
	v_fmac_f32_e32 v16, v22, v24
	v_fmac_f32_e32 v17, v20, v26
	v_add_f32_e32 v16, v16, v17
	v_add_f32_e32 v20, v28, v16
	ds_read_b128 v[16:19], v93 offset:63488
	v_add_f32_e32 v104, v104, v105
	ds_swizzle_b32 v105, v104 offset:swizzle(SWAP,16)
	v_add_f32_e32 v102, v102, v103
	v_mov_b32_e32 v99, v98
	s_waitcnt lgkmcnt(1)
	v_mul_f32_e32 v15, v15, v17
	v_mul_f32_e32 v13, v13, v19
	v_fmac_f32_e32 v15, v14, v16
	v_fmac_f32_e32 v13, v12, v18
	v_mul_f32_e32 v21, v39, v17
	v_add_f32_e32 v12, v15, v13
	v_fmac_f32_e32 v21, v38, v16
	v_add_f32_e32 v16, v20, v12
	ds_read_b128 v[12:15], v93 offset:64512
	v_mul_f32_e32 v22, v37, v19
	v_fmac_f32_e32 v22, v36, v18
	v_add_f32_e32 v21, v21, v22
	v_add_f32_e32 v21, v29, v21
	s_waitcnt lgkmcnt(0)
	v_mul_f32_e32 v5, v5, v13
	v_mul_f32_e32 v1, v1, v15
	v_fmac_f32_e32 v5, v4, v12
	v_fmac_f32_e32 v1, v0, v14
	v_add_f32_e32 v0, v5, v1
	v_mul_f32_e32 v1, v7, v13
	v_mul_f32_e32 v3, v3, v15
	v_fmac_f32_e32 v1, v6, v12
	v_fmac_f32_e32 v3, v2, v14
	v_add_f32_e32 v1, v1, v3
	v_add_f32_e32 v0, v21, v0
	v_add_f32_e32 v2, v16, v1
	ds_swizzle_b32 v1, v0 offset:swizzle(SWAP,1)
	ds_swizzle_b32 v3, v2 offset:swizzle(SWAP,1)
	v_add_f32_e32 v104, v104, v105
	v_mov_b32_e32 v101, v100
	v_mov_b32_e32 v103, v102
	s_waitcnt lgkmcnt(1)
	v_add_f32_e32 v0, v0, v1
	s_waitcnt lgkmcnt(0)
	v_add_f32_e32 v2, v2, v3
	ds_swizzle_b32 v1, v0 offset:swizzle(SWAP,2)
	ds_swizzle_b32 v3, v2 offset:swizzle(SWAP,2)
	v_mov_b32_e32 v105, v104
	v_permlane32_swap_b32_e32 v64, v65
	s_waitcnt lgkmcnt(1)
	v_add_f32_e32 v0, v0, v1
	s_waitcnt lgkmcnt(0)
	v_add_f32_e32 v2, v2, v3
	ds_swizzle_b32 v1, v0 offset:swizzle(SWAP,4)
	ds_swizzle_b32 v3, v2 offset:swizzle(SWAP,4)
	v_permlane32_swap_b32_e32 v66, v67
	v_permlane32_swap_b32_e32 v68, v69
	s_waitcnt lgkmcnt(1)
	v_add_f32_e32 v0, v0, v1
	s_waitcnt lgkmcnt(0)
	v_add_f32_e32 v2, v2, v3
	ds_swizzle_b32 v1, v0 offset:swizzle(SWAP,8)
	ds_swizzle_b32 v3, v2 offset:swizzle(SWAP,8)
	v_permlane32_swap_b32_e32 v70, v71
	v_permlane32_swap_b32_e32 v85, v90
	s_waitcnt lgkmcnt(1)
	v_add_f32_e32 v0, v0, v1
	s_waitcnt lgkmcnt(0)
	v_add_f32_e32 v2, v2, v3
	ds_swizzle_b32 v1, v0 offset:swizzle(SWAP,16)
	ds_swizzle_b32 v3, v2 offset:swizzle(SWAP,16)
	v_permlane32_swap_b32_e32 v91, v92
	v_permlane32_swap_b32_e32 v94, v95
	s_waitcnt lgkmcnt(1)
	v_add_f32_e32 v0, v0, v1
	s_waitcnt lgkmcnt(0)
	v_add_f32_e32 v2, v2, v3
	v_mov_b32_e32 v1, v0
	v_mov_b32_e32 v3, v2
	v_permlane32_swap_b32_e32 v96, v97
	v_permlane32_swap_b32_e32 v98, v99
	v_permlane32_swap_b32_e32 v100, v101
	v_permlane32_swap_b32_e32 v102, v103
	v_permlane32_swap_b32_e32 v104, v105
	v_permlane32_swap_b32_e32 v0, v1
	v_permlane32_swap_b32_e32 v2, v3
	s_and_saveexec_b64 s[40:41], s[2:3]
	s_cbranch_execz .LBB0_99
	v_add_f32_e32 v10, v10, v11
	v_add_f32_e32 v8, v8, v9
	v_add_f32_e32 v16, v66, v67
	v_add_f32_e32 v17, v64, v65
	v_cndmask_b32_e64 v8, v8, v10, s[4:5]
	v_add_f32_e32 v14, v70, v71
	v_add_f32_e32 v15, v68, v69
	v_cndmask_b32_e64 v8, 0, v8, s[8:9]
	v_cndmask_b32_e64 v9, v17, v16, s[4:5]
	v_add_f32_e32 v12, v91, v92
	v_add_f32_e32 v13, v85, v90
	v_cndmask_b32_e64 v8, v8, v9, s[10:11]
	v_cndmask_b32_e64 v9, v15, v14, s[4:5]
	v_add_f32_e32 v6, v96, v97
	v_add_f32_e32 v7, v94, v95
	v_cndmask_b32_e64 v8, v8, v9, s[12:13]
	v_cndmask_b32_e64 v9, v13, v12, s[4:5]
	v_add_f32_e32 v4, v100, v101
	v_add_f32_e32 v5, v98, v99
	v_cndmask_b32_e64 v8, v8, v9, s[14:15]
	v_cndmask_b32_e64 v6, v7, v6, s[4:5]
	v_add_f32_e32 v2, v2, v3
	v_add_f32_e32 v0, v0, v1
	v_add_f32_e32 v1, v104, v105
	v_add_f32_e32 v3, v102, v103
	v_cndmask_b32_e64 v6, v8, v6, s[16:17]
	v_cndmask_b32_e64 v4, v5, v4, s[4:5]
	v_cndmask_b32_e64 v4, v6, v4, s[18:19]
	v_cndmask_b32_e64 v1, v3, v1, s[4:5]
	v_cndmask_b32_e64 v1, v4, v1, s[20:21]
	v_cndmask_b32_e64 v0, v0, v2, s[4:5]
	v_cndmask_b32_e64 v1, v1, v0, s[22:23]
	s_and_saveexec_b64 s[24:25], s[6:7]
	s_xor_b64 s[42:43], exec, s[24:25]
	s_cbranch_execz .LBB0_108
	flat_load_dword v0, v[78:79]
	s_mov_b32 s24, 0xbfb8aa3b
	s_waitcnt vmcnt(0) lgkmcnt(0)
	v_add_f32_e32 v0, v1, v0
	v_mul_f32_e64 v1, |v0|, s24
	v_exp_f32_e32 v1, v1
	s_nop 0
	v_add_f32_e32 v3, 1.0, v1
	v_add_f32_e32 v2, -1.0, v3
	v_cmp_neq_f32_e32 vcc, 0, v2
	s_and_saveexec_b64 s[44:45], vcc
	s_cbranch_execz .LBB0_107
	s_mov_b32 s24, 0x800000
	v_cmp_gt_f32_e32 vcc, s24, v3
	s_nop 1
	v_cndmask_b32_e64 v4, 0, 32, vcc
	v_ldexp_f32 v3, v3, v4
	v_log_f32_e32 v3, v3
	v_div_scale_f32 v4, s[24:25], v2, v2, v1
	s_mov_b32 s24, 0x3f317217
	v_mul_f32_e32 v5, 0x3f317217, v3
	v_fma_f32 v5, v3, s24, -v5
	v_fmac_f32_e32 v5, 0x3377d1cf, v3
	v_rcp_f32_e32 v6, v4
	s_mov_b32 s24, 0x7f800000
	v_fmac_f32_e32 v5, 0x3f317217, v3
	v_cmp_lt_f32_e64 s[24:25], |v3|, s24
	s_nop 1
	v_cndmask_b32_e64 v3, v3, v5, s[24:25]
	v_mov_b32_e32 v5, 0x41b17218
	v_cndmask_b32_e32 v5, 0, v5, vcc
	v_sub_f32_e32 v3, v3, v5
	v_fma_f32 v5, -v4, v6, 1.0
	v_fmac_f32_e32 v6, v5, v6
	v_div_scale_f32 v5, vcc, v1, v2, v1
	v_mul_f32_e32 v7, v5, v6
	v_fma_f32 v8, -v4, v7, v5
	v_fmac_f32_e32 v7, v8, v6
	v_fma_f32 v4, -v4, v7, v5
	v_div_fmas_f32 v4, v4, v6, v7
	v_div_fixup_f32 v1, v4, v2, v1
	v_mul_f32_e32 v1, v3, v1

.LBB0_551:
	v_add_f32_e32 v162, v144, v145
	v_fmac_f32_e32 v162, v178, v160
	v_mul_u32_u24_e32 v160, 0x6800, v176
	ds_read_b64_tr_b16 v[144:145], v177 offset:0x8000
	ds_read_b64_tr_b16 v[146:147], v177 offset:0x9000
	ds_read_b64_tr_b16 v[148:149], v177 offset:0xa000
	ds_read_b64_tr_b16 v[150:151], v177 offset:0xb000
	ds_read_b64_tr_b16 v[152:153], v177 offset:0xc000
	ds_read_b64_tr_b16 v[154:155], v177 offset:0xd000
	ds_read_b64_tr_b16 v[156:157], v177 offset:0xe000
	ds_read_b64_tr_b16 v[158:159], v177 offset:0xf000
	ds_read_b64_tr_b16 v[166:167], v177 offset:0x8200
	ds_read_b64_tr_b16 v[168:169], v177 offset:0x9200
	ds_read_b64_tr_b16 v[178:179], v177 offset:0xa200
	ds_read_b64_tr_b16 v[180:181], v177 offset:0xb200
	ds_read_b64_tr_b16 v[182:183], v177 offset:0xc200
	ds_read_b64_tr_b16 v[184:185], v177 offset:0xd200
	ds_read_b64_tr_b16 v[186:187], v177 offset:0xe200
	ds_read_b64_tr_b16 v[188:189], v177 offset:0xf200
	s_waitcnt lgkmcnt(8)
	s_nop 0
	v_mfma_f32_32x32x16_bf16 v[112:127], v[144:147], v[128:131], v[112:127]
	v_mfma_f32_32x32x16_bf16 v[112:127], v[148:151], v[132:135], v[112:127]
	v_mfma_f32_32x32x16_bf16 v[112:127], v[152:155], v[136:139], v[112:127]
	v_mfma_f32_32x32x16_bf16 v[112:127], v[156:159], v[140:143], v[112:127]
	ds_read_b64_tr_b16 v[144:145], v177 offset:0x8400
	ds_read_b64_tr_b16 v[146:147], v177 offset:0x9400
	ds_read_b64_tr_b16 v[148:149], v177 offset:0xa400
	ds_read_b64_tr_b16 v[150:151], v177 offset:0xb400
	ds_read_b64_tr_b16 v[152:153], v177 offset:0xc400
	ds_read_b64_tr_b16 v[154:155], v177 offset:0xd400
	ds_read_b64_tr_b16 v[156:157], v177 offset:0xe400
	ds_read_b64_tr_b16 v[158:159], v177 offset:0xf400
	s_waitcnt lgkmcnt(8)
	v_mfma_f32_32x32x16_bf16 v[96:111], v[166:169], v[128:131], v[96:111]
	v_mfma_f32_32x32x16_bf16 v[96:111], v[178:181], v[132:135], v[96:111]
	v_mfma_f32_32x32x16_bf16 v[96:111], v[182:185], v[136:139], v[96:111]
	v_mfma_f32_32x32x16_bf16 v[96:111], v[186:189], v[140:143], v[96:111]
	ds_read_b64_tr_b16 v[166:167], v177 offset:0x8600
	ds_read_b64_tr_b16 v[168:169], v177 offset:0x9600
	ds_read_b64_tr_b16 v[178:179], v177 offset:0xa600
	ds_read_b64_tr_b16 v[180:181], v177 offset:0xb600
	ds_read_b64_tr_b16 v[182:183], v177 offset:0xc600
	ds_read_b64_tr_b16 v[184:185], v177 offset:0xd600
	ds_read_b64_tr_b16 v[186:187], v177 offset:0xe600
	ds_read_b64_tr_b16 v[188:189], v177 offset:0xf600
	s_waitcnt lgkmcnt(8)
	v_mfma_f32_32x32x16_bf16 v[80:95], v[144:147], v[128:131], v[80:95]
	v_mfma_f32_32x32x16_bf16 v[80:95], v[148:151], v[132:135], v[80:95]
	v_mfma_f32_32x32x16_bf16 v[80:95], v[152:155], v[136:139], v[80:95]
	v_mfma_f32_32x32x16_bf16 v[80:95], v[156:159], v[140:143], v[80:95]
	ds_read_b64_tr_b16 v[144:145], v177 offset:0x8800
	ds_read_b64_tr_b16 v[146:147], v177 offset:0x9800
	ds_read_b64_tr_b16 v[148:149], v177 offset:0xa800
	ds_read_b64_tr_b16 v[150:151], v177 offset:0xb800
	ds_read_b64_tr_b16 v[152:153], v177 offset:0xc800
	ds_read_b64_tr_b16 v[154:155], v177 offset:0xd800
	ds_read_b64_tr_b16 v[156:157], v177 offset:0xe800
	ds_read_b64_tr_b16 v[158:159], v177 offset:0xf800
	s_waitcnt lgkmcnt(8)
	v_mfma_f32_32x32x16_bf16 v[64:79], v[166:169], v[128:131], v[64:79]
	v_mfma_f32_32x32x16_bf16 v[64:79], v[178:181], v[132:135], v[64:79]
	v_mfma_f32_32x32x16_bf16 v[64:79], v[182:185], v[136:139], v[64:79]
	v_mfma_f32_32x32x16_bf16 v[64:79], v[186:189], v[140:143], v[64:79]
	ds_read_b64_tr_b16 v[166:167], v177 offset:0x8a00
	ds_read_b64_tr_b16 v[168:169], v177 offset:0x9a00
	ds_read_b64_tr_b16 v[178:179], v177 offset:0xaa00
	ds_read_b64_tr_b16 v[180:181], v177 offset:0xba00
	ds_read_b64_tr_b16 v[182:183], v177 offset:0xca00
	ds_read_b64_tr_b16 v[184:185], v177 offset:0xda00
	ds_read_b64_tr_b16 v[186:187], v177 offset:0xea00
	ds_read_b64_tr_b16 v[188:189], v177 offset:0xfa00
	s_waitcnt lgkmcnt(8)
	v_mfma_f32_32x32x16_bf16 v[48:63], v[144:147], v[128:131], v[48:63]
	v_mfma_f32_32x32x16_bf16 v[48:63], v[148:151], v[132:135], v[48:63]
	v_mfma_f32_32x32x16_bf16 v[48:63], v[152:155], v[136:139], v[48:63]
	v_mfma_f32_32x32x16_bf16 v[48:63], v[156:159], v[140:143], v[48:63]
	ds_read_b64_tr_b16 v[144:145], v177 offset:0x8c00
	ds_read_b64_tr_b16 v[146:147], v177 offset:0x9c00
	ds_read_b64_tr_b16 v[148:149], v177 offset:0xac00
	ds_read_b64_tr_b16 v[150:151], v177 offset:0xbc00
	ds_read_b64_tr_b16 v[152:153], v177 offset:0xcc00
	ds_read_b64_tr_b16 v[154:155], v177 offset:0xdc00
	ds_read_b64_tr_b16 v[156:157], v177 offset:0xec00
	ds_read_b64_tr_b16 v[158:159], v177 offset:0xfc00
	s_waitcnt lgkmcnt(8)
	v_mfma_f32_32x32x16_bf16 v[32:47], v[166:169], v[128:131], v[32:47]
	v_mfma_f32_32x32x16_bf16 v[32:47], v[178:181], v[132:135], v[32:47]
	v_mfma_f32_32x32x16_bf16 v[32:47], v[182:185], v[136:139], v[32:47]
	v_mfma_f32_32x32x16_bf16 v[32:47], v[186:189], v[140:143], v[32:47]
	ds_read_b64_tr_b16 v[166:167], v177 offset:0x8e00
	ds_read_b64_tr_b16 v[168:169], v177 offset:0x9e00
	ds_read_b64_tr_b16 v[178:179], v177 offset:0xae00
	ds_read_b64_tr_b16 v[180:181], v177 offset:0xbe00
	ds_read_b64_tr_b16 v[182:183], v177 offset:0xce00
	ds_read_b64_tr_b16 v[184:185], v177 offset:0xde00
	ds_read_b64_tr_b16 v[186:187], v177 offset:0xee00
	ds_read_b64_tr_b16 v[188:189], v177 offset:0xfe00
	s_waitcnt lgkmcnt(8)
	v_mfma_f32_32x32x16_bf16 v[16:31], v[144:147], v[128:131], v[16:31]
	v_mfma_f32_32x32x16_bf16 v[16:31], v[148:151], v[132:135], v[16:31]
	v_mfma_f32_32x32x16_bf16 v[16:31], v[152:155], v[136:139], v[16:31]
	v_mfma_f32_32x32x16_bf16 v[16:31], v[156:159], v[140:143], v[16:31]
	s_waitcnt lgkmcnt(0)
	v_mfma_f32_32x32x16_bf16 v[0:15], v[166:169], v[128:131], v[0:15]
	v_mfma_f32_32x32x16_bf16 v[0:15], v[178:181], v[132:135], v[0:15]
	v_mfma_f32_32x32x16_bf16 v[0:15], v[182:185], v[136:139], v[0:15]
	v_mfma_f32_32x32x16_bf16 v[0:15], v[186:189], v[140:143], v[0:15]
	v_readlane_b32 s2, v255, 46
	v_readlane_b32 s3, v255, 47
	s_ashr_i32 s93, s92, 31
	v_or_b32_e32 v160, v175, v160
	v_mov_b64_e32 v[128:129], s[2:3]
	v_readlane_b32 s2, v255, 54
	v_readlane_b32 s3, v255, 55
	flat_load_dword v130, v[128:129] sc0 sc1
	s_waitcnt vmcnt(0) lgkmcnt(0)
	v_readfirstlane_b32 s4, v130
	v_mov_b64_e32 v[128:129], s[2:3]
	flat_load_dword v128, v[128:129] sc0 sc1
	s_waitcnt vmcnt(0)
	s_mul_i32 s3, s92, 0x6800
	s_mul_hi_i32 s2, s92, 0x6800
	s_add_u32 s4, s4, s3
	s_waitcnt lgkmcnt(0)
	s_barrier
	s_waitcnt lgkmcnt(0)
	v_readfirstlane_b32 s5, v128
	s_addc_u32 s5, s5, s2
	s_nop 0
	v_lshl_add_u64 v[156:157], s[4:5], 0, v[160:161]
	flat_load_dwordx4 v[128:131], v[156:157]
	flat_load_dwordx4 v[132:135], v[156:157] offset:32
	flat_load_dwordx4 v[136:139], v[156:157] offset:64
	flat_load_dwordx4 v[140:143], v[156:157] offset:96
	flat_load_dwordx4 v[144:147], v[156:157] offset:128
	flat_load_dwordx4 v[148:151], v[156:157] offset:160
	flat_load_dwordx4 v[152:155], v[156:157] offset:192
	flat_load_dwordx4 v[166:169], v[156:157] offset:224
	s_lshl_b64 s[4:5], s[92:93], 12
	s_add_u32 s4, s83, s4
	v_rcp_f32_e32 v159, v162
	s_addc_u32 s5, s95, s5
	v_lshl_or_b32 v162, v176, 12, v175
	global_load_dwordx4 v[194:197], v162, s[4:5]
	global_load_dwordx4 v[198:201], v162, s[4:5] offset:32
	global_load_dwordx4 v[202:205], v162, s[4:5] offset:64
	global_load_dwordx4 v[206:209], v162, s[4:5] offset:96
	global_load_dwordx4 v[210:213], v162, s[4:5] offset:128
	global_load_dwordx4 v[214:217], v162, s[4:5] offset:160
	global_load_dwordx4 v[218:221], v162, s[4:5] offset:192
	global_load_dwordx4 v[222:225], v162, s[4:5] offset:224
	v_mul_f32_e32 v112, v159, v112
	v_mul_f32_e32 v96, v159, v96
	v_mul_f32_e32 v80, v159, v80
	v_mul_f32_e32 v64, v159, v64
	v_mul_f32_e32 v48, v159, v48
	v_mul_f32_e32 v32, v159, v32
	v_mul_f32_e32 v16, v159, v16
	v_mul_f32_e32 v0, v159, v0
	v_readlane_b32 s18, v255, 19
	s_waitcnt vmcnt(0)
	v_mov_b32_e32 v163, v196
	s_nop 1
	v_permlane32_swap_b32_e32 v194, v163
	v_mov_b32_e32 v170, v197
	v_fma_mix_f32 v157, -v174, v112, v194 op_sel_hi:[0,0,1]
	v_mul_f32_e32 v112, v159, v113
	v_permlane32_swap_b32_e32 v195, v170
	v_fma_mix_f32 v156, -v174, v112, v194 op_sel:[0,0,1] op_sel_hi:[0,0,1]
	v_mul_f32_e32 v112, v159, v114
	v_fma_mix_f32 v113, -v174, v112, v195 op_sel_hi:[0,0,1]
	v_mul_f32_e32 v112, v159, v115
	v_fma_mix_f32 v112, -v174, v112, v195 op_sel:[0,0,1] op_sel_hi:[0,0,1]
	global_load_dwordx4 v[194:197], v162, s[4:5] offset:256
	v_mul_f32_e32 v114, v159, v116
	v_fma_mix_f32 v158, -v174, v114, v163 op_sel_hi:[0,0,1]
	v_mul_f32_e32 v114, v159, v117
	v_fma_mix_f32 v116, -v174, v114, v163 op_sel:[0,0,1] op_sel_hi:[0,0,1]
	v_mul_f32_e32 v114, v159, v118
	v_fma_mix_f32 v115, -v174, v114, v170 op_sel_hi:[0,0,1]
	v_mul_f32_e32 v114, v159, v119
	v_mul_f32_e32 v117, v159, v120
	v_fma_mix_f32 v114, -v174, v114, v170 op_sel:[0,0,1] op_sel_hi:[0,0,1]
	s_waitcnt vmcnt(7)
	v_mov_b32_e32 v163, v200
	s_nop 1
	v_permlane32_swap_b32_e32 v198, v163
	v_mov_b32_e32 v170, v201
	v_fma_mix_f32 v120, -v174, v117, v198 op_sel_hi:[0,0,1]
	v_mul_f32_e32 v117, v159, v121
	v_permlane32_swap_b32_e32 v199, v170
	v_fma_mix_f32 v119, -v174, v117, v198 op_sel:[0,0,1] op_sel_hi:[0,0,1]
	v_mul_f32_e32 v117, v159, v122
	v_fma_mix_f32 v118, -v174, v117, v199 op_sel_hi:[0,0,1]
	v_mul_f32_e32 v117, v159, v123
	v_fma_mix_f32 v117, -v174, v117, v199 op_sel:[0,0,1] op_sel_hi:[0,0,1]
	global_load_dwordx4 v[198:201], v162, s[4:5] offset:288
	v_mul_f32_e32 v121, v159, v124
	v_fma_mix_f32 v124, -v174, v121, v163 op_sel_hi:[0,0,1]
	v_mul_f32_e32 v121, v159, v125
	v_fma_mix_f32 v123, -v174, v121, v163 op_sel:[0,0,1] op_sel_hi:[0,0,1]
	v_mul_f32_e32 v121, v159, v126
	v_fma_mix_f32 v122, -v174, v121, v170 op_sel_hi:[0,0,1]
	v_mul_f32_e32 v121, v159, v127
	v_fma_mix_f32 v121, -v174, v121, v170 op_sel:[0,0,1] op_sel_hi:[0,0,1]
	s_waitcnt vmcnt(7)
	v_mov_b32_e32 v163, v204
	s_nop 1
	v_permlane32_swap_b32_e32 v202, v163
	v_mov_b32_e32 v170, v205
	v_fma_mix_f32 v126, -v174, v96, v202 op_sel_hi:[0,0,1]
	v_mul_f32_e32 v96, v159, v97
	v_permlane32_swap_b32_e32 v203, v170
	v_fma_mix_f32 v125, -v174, v96, v202 op_sel:[0,0,1] op_sel_hi:[0,0,1]
	v_mul_f32_e32 v96, v159, v98
	v_fma_mix_f32 v97, -v174, v96, v203 op_sel_hi:[0,0,1]
	v_mul_f32_e32 v96, v159, v99
	v_fma_mix_f32 v96, -v174, v96, v203 op_sel:[0,0,1] op_sel_hi:[0,0,1]
	global_load_dwordx4 v[202:205], v162, s[4:5] offset:320
	v_mul_f32_e32 v98, v159, v100
	v_fma_mix_f32 v127, -v174, v98, v163 op_sel_hi:[0,0,1]
	v_mul_f32_e32 v98, v159, v101
	v_fma_mix_f32 v100, -v174, v98, v163 op_sel:[0,0,1] op_sel_hi:[0,0,1]
	v_mul_f32_e32 v98, v159, v102
	v_fma_mix_f32 v99, -v174, v98, v170 op_sel_hi:[0,0,1]
	v_mul_f32_e32 v98, v159, v103
	v_mul_f32_e32 v101, v159, v104
	v_fma_mix_f32 v98, -v174, v98, v170 op_sel:[0,0,1] op_sel_hi:[0,0,1]
	s_waitcnt vmcnt(7)
	v_mov_b32_e32 v163, v208
	s_nop 1
	v_permlane32_swap_b32_e32 v206, v163
	v_mov_b32_e32 v170, v209
	v_fma_mix_f32 v104, -v174, v101, v206 op_sel_hi:[0,0,1]
	v_mul_f32_e32 v101, v159, v105
	v_permlane32_swap_b32_e32 v207, v170
	v_fma_mix_f32 v103, -v174, v101, v206 op_sel:[0,0,1] op_sel_hi:[0,0,1]
	v_mul_f32_e32 v101, v159, v106
	v_fma_mix_f32 v102, -v174, v101, v207 op_sel_hi:[0,0,1]
	v_mul_f32_e32 v101, v159, v107
	v_fma_mix_f32 v101, -v174, v101, v207 op_sel:[0,0,1] op_sel_hi:[0,0,1]
	global_load_dwordx4 v[206:209], v162, s[4:5] offset:352
	v_mul_f32_e32 v105, v159, v108
	v_fma_mix_f32 v108, -v174, v105, v163 op_sel_hi:[0,0,1]
	v_mul_f32_e32 v105, v159, v109
	v_fma_mix_f32 v107, -v174, v105, v163 op_sel:[0,0,1] op_sel_hi:[0,0,1]
	v_mul_f32_e32 v105, v159, v110
	v_fma_mix_f32 v106, -v174, v105, v170 op_sel_hi:[0,0,1]
	v_mul_f32_e32 v105, v159, v111
	v_fma_mix_f32 v105, -v174, v105, v170 op_sel:[0,0,1] op_sel_hi:[0,0,1]
	s_waitcnt vmcnt(7)
	v_mov_b32_e32 v163, v212
	s_nop 1
	v_permlane32_swap_b32_e32 v210, v163
	v_mov_b32_e32 v170, v213
	v_fma_mix_f32 v110, -v174, v80, v210 op_sel_hi:[0,0,1]
	v_mul_f32_e32 v80, v159, v81
	v_permlane32_swap_b32_e32 v211, v170
	v_fma_mix_f32 v109, -v174, v80, v210 op_sel:[0,0,1] op_sel_hi:[0,0,1]
	v_mul_f32_e32 v80, v159, v82
	v_fma_mix_f32 v81, -v174, v80, v211 op_sel_hi:[0,0,1]
	v_mul_f32_e32 v80, v159, v83
	v_fma_mix_f32 v80, -v174, v80, v211 op_sel:[0,0,1] op_sel_hi:[0,0,1]
	global_load_dwordx4 v[210:213], v162, s[4:5] offset:384
	v_mul_f32_e32 v82, v159, v84
	v_fma_mix_f32 v111, -v174, v82, v163 op_sel_hi:[0,0,1]
	v_mul_f32_e32 v82, v159, v85
	v_fma_mix_f32 v84, -v174, v82, v163 op_sel:[0,0,1] op_sel_hi:[0,0,1]
	v_mul_f32_e32 v82, v159, v86
	v_fma_mix_f32 v83, -v174, v82, v170 op_sel_hi:[0,0,1]
	v_mul_f32_e32 v82, v159, v87
	v_mul_f32_e32 v85, v159, v88
	v_fma_mix_f32 v82, -v174, v82, v170 op_sel:[0,0,1] op_sel_hi:[0,0,1]
	s_waitcnt vmcnt(7)
	v_mov_b32_e32 v163, v216
	s_nop 1
	v_permlane32_swap_b32_e32 v214, v163
	v_mov_b32_e32 v170, v217
	v_fma_mix_f32 v88, -v174, v85, v214 op_sel_hi:[0,0,1]
	v_mul_f32_e32 v85, v159, v89
	v_permlane32_swap_b32_e32 v215, v170
	v_fma_mix_f32 v87, -v174, v85, v214 op_sel:[0,0,1] op_sel_hi:[0,0,1]
	v_mul_f32_e32 v85, v159, v90
	v_fma_mix_f32 v86, -v174, v85, v215 op_sel_hi:[0,0,1]
	v_mul_f32_e32 v85, v159, v91
	v_fma_mix_f32 v85, -v174, v85, v215 op_sel:[0,0,1] op_sel_hi:[0,0,1]
	global_load_dwordx4 v[214:217], v162, s[4:5] offset:416
	v_mul_f32_e32 v89, v159, v92
	v_fma_mix_f32 v92, -v174, v89, v163 op_sel_hi:[0,0,1]
	v_mul_f32_e32 v89, v159, v93
	v_fma_mix_f32 v91, -v174, v89, v163 op_sel:[0,0,1] op_sel_hi:[0,0,1]
	v_mul_f32_e32 v89, v159, v94
	v_fma_mix_f32 v90, -v174, v89, v170 op_sel_hi:[0,0,1]
	v_mul_f32_e32 v89, v159, v95
	v_fma_mix_f32 v89, -v174, v89, v170 op_sel:[0,0,1] op_sel_hi:[0,0,1]
	s_waitcnt vmcnt(7)
	v_mov_b32_e32 v163, v220
	s_nop 1
	v_permlane32_swap_b32_e32 v218, v163
	v_mov_b32_e32 v170, v221
	v_fma_mix_f32 v94, -v174, v64, v218 op_sel_hi:[0,0,1]
	v_mul_f32_e32 v64, v159, v65
	v_permlane32_swap_b32_e32 v219, v170
	v_fma_mix_f32 v93, -v174, v64, v218 op_sel:[0,0,1] op_sel_hi:[0,0,1]
	v_mul_f32_e32 v64, v159, v66
	v_fma_mix_f32 v65, -v174, v64, v219 op_sel_hi:[0,0,1]
	v_mul_f32_e32 v64, v159, v67
	v_fma_mix_f32 v64, -v174, v64, v219 op_sel:[0,0,1] op_sel_hi:[0,0,1]
	global_load_dwordx4 v[218:221], v162, s[4:5] offset:448
	v_mul_f32_e32 v66, v159, v68
	v_fma_mix_f32 v95, -v174, v66, v163 op_sel_hi:[0,0,1]
	v_mul_f32_e32 v66, v159, v69
	v_fma_mix_f32 v68, -v174, v66, v163 op_sel:[0,0,1] op_sel_hi:[0,0,1]
	v_mul_f32_e32 v66, v159, v70
	v_fma_mix_f32 v67, -v174, v66, v170 op_sel_hi:[0,0,1]
	v_mul_f32_e32 v66, v159, v71
	v_mul_f32_e32 v69, v159, v72
	v_fma_mix_f32 v66, -v174, v66, v170 op_sel:[0,0,1] op_sel_hi:[0,0,1]
	s_waitcnt vmcnt(7)
	v_mov_b32_e32 v163, v224
	s_nop 1
	v_permlane32_swap_b32_e32 v222, v163
	v_mov_b32_e32 v170, v225
	v_fma_mix_f32 v72, -v174, v69, v222 op_sel_hi:[0,0,1]
	v_mul_f32_e32 v69, v159, v73
	v_permlane32_swap_b32_e32 v223, v170
	v_fma_mix_f32 v71, -v174, v69, v222 op_sel:[0,0,1] op_sel_hi:[0,0,1]
	v_mul_f32_e32 v69, v159, v74
	v_fma_mix_f32 v70, -v174, v69, v223 op_sel_hi:[0,0,1]
	v_mul_f32_e32 v69, v159, v75
	v_fma_mix_f32 v69, -v174, v69, v223 op_sel:[0,0,1] op_sel_hi:[0,0,1]
	v_mul_f32_e32 v73, v159, v76
	v_fma_mix_f32 v76, -v174, v73, v163 op_sel_hi:[0,0,1]
	v_mul_f32_e32 v73, v159, v77
	v_fma_mix_f32 v75, -v174, v73, v163 op_sel:[0,0,1] op_sel_hi:[0,0,1]
	v_mul_f32_e32 v73, v159, v78
	v_fma_mix_f32 v74, -v174, v73, v170 op_sel_hi:[0,0,1]
	v_mul_f32_e32 v73, v159, v79
	v_fma_mix_f32 v73, -v174, v73, v170 op_sel:[0,0,1] op_sel_hi:[0,0,1]
	s_waitcnt vmcnt(6)
	v_mov_b32_e32 v163, v196
	s_nop 1
	v_permlane32_swap_b32_e32 v194, v163
	v_mov_b32_e32 v170, v197
	v_fma_mix_f32 v78, -v174, v48, v194 op_sel_hi:[0,0,1]
	v_mul_f32_e32 v48, v159, v49
	v_permlane32_swap_b32_e32 v195, v170
	v_fma_mix_f32 v77, -v174, v48, v194 op_sel:[0,0,1] op_sel_hi:[0,0,1]
	v_mul_f32_e32 v48, v159, v50
	v_fma_mix_f32 v49, -v174, v48, v195 op_sel_hi:[0,0,1]
	v_mul_f32_e32 v48, v159, v51
	v_fma_mix_f32 v48, -v174, v48, v195 op_sel:[0,0,1] op_sel_hi:[0,0,1]
	v_mul_f32_e32 v50, v159, v52
	v_fma_mix_f32 v79, -v174, v50, v163 op_sel_hi:[0,0,1]
	v_mul_f32_e32 v50, v159, v53
	v_fma_mix_f32 v52, -v174, v50, v163 op_sel:[0,0,1] op_sel_hi:[0,0,1]
	v_mul_f32_e32 v50, v159, v54
	v_fma_mix_f32 v51, -v174, v50, v170 op_sel_hi:[0,0,1]
	v_mul_f32_e32 v50, v159, v55
	v_mul_f32_e32 v53, v159, v56
	v_fma_mix_f32 v50, -v174, v50, v170 op_sel:[0,0,1] op_sel_hi:[0,0,1]
	s_waitcnt vmcnt(5)
	v_mov_b32_e32 v163, v200
	s_nop 1
	v_permlane32_swap_b32_e32 v198, v163
	v_mov_b32_e32 v170, v201
	v_fma_mix_f32 v56, -v174, v53, v198 op_sel_hi:[0,0,1]
	v_mul_f32_e32 v53, v159, v57
	v_permlane32_swap_b32_e32 v199, v170
	v_fma_mix_f32 v55, -v174, v53, v198 op_sel:[0,0,1] op_sel_hi:[0,0,1]
	v_mul_f32_e32 v53, v159, v58
	v_fma_mix_f32 v54, -v174, v53, v199 op_sel_hi:[0,0,1]
	v_mul_f32_e32 v53, v159, v59
	v_fma_mix_f32 v53, -v174, v53, v199 op_sel:[0,0,1] op_sel_hi:[0,0,1]
	v_mul_f32_e32 v57, v159, v60
	v_fma_mix_f32 v60, -v174, v57, v163 op_sel_hi:[0,0,1]
	v_mul_f32_e32 v57, v159, v61
	v_fma_mix_f32 v59, -v174, v57, v163 op_sel:[0,0,1] op_sel_hi:[0,0,1]
	v_mul_f32_e32 v57, v159, v62
	v_fma_mix_f32 v58, -v174, v57, v170 op_sel_hi:[0,0,1]
	v_mul_f32_e32 v57, v159, v63
	v_fma_mix_f32 v57, -v174, v57, v170 op_sel:[0,0,1] op_sel_hi:[0,0,1]
	s_waitcnt vmcnt(4)
	v_mov_b32_e32 v163, v204
	s_nop 1
	v_permlane32_swap_b32_e32 v202, v163
	v_mov_b32_e32 v170, v205
	v_fma_mix_f32 v62, -v174, v32, v202 op_sel_hi:[0,0,1]
	v_mul_f32_e32 v32, v159, v33
	v_permlane32_swap_b32_e32 v203, v170
	v_fma_mix_f32 v61, -v174, v32, v202 op_sel:[0,0,1] op_sel_hi:[0,0,1]
	v_mul_f32_e32 v32, v159, v34
	v_fma_mix_f32 v33, -v174, v32, v203 op_sel_hi:[0,0,1]
	v_mul_f32_e32 v32, v159, v35
	v_fma_mix_f32 v32, -v174, v32, v203 op_sel:[0,0,1] op_sel_hi:[0,0,1]
	v_mul_f32_e32 v34, v159, v36
	v_fma_mix_f32 v63, -v174, v34, v163 op_sel_hi:[0,0,1]
	v_mul_f32_e32 v34, v159, v37
	v_fma_mix_f32 v36, -v174, v34, v163 op_sel:[0,0,1] op_sel_hi:[0,0,1]
	v_mul_f32_e32 v34, v159, v38
	v_fma_mix_f32 v35, -v174, v34, v170 op_sel_hi:[0,0,1]
	v_mul_f32_e32 v34, v159, v39
	v_mul_f32_e32 v37, v159, v40
	v_fma_mix_f32 v34, -v174, v34, v170 op_sel:[0,0,1] op_sel_hi:[0,0,1]
	s_waitcnt vmcnt(3)
	v_mov_b32_e32 v163, v208
	s_nop 1
	v_permlane32_swap_b32_e32 v206, v163
	v_mov_b32_e32 v170, v209
	v_fma_mix_f32 v40, -v174, v37, v206 op_sel_hi:[0,0,1]
	v_mul_f32_e32 v37, v159, v41
	v_permlane32_swap_b32_e32 v207, v170
	v_fma_mix_f32 v39, -v174, v37, v206 op_sel:[0,0,1] op_sel_hi:[0,0,1]
	v_mul_f32_e32 v37, v159, v42
	v_fma_mix_f32 v38, -v174, v37, v207 op_sel_hi:[0,0,1]
	v_mul_f32_e32 v37, v159, v43
	v_fma_mix_f32 v37, -v174, v37, v207 op_sel:[0,0,1] op_sel_hi:[0,0,1]
	v_mul_f32_e32 v41, v159, v44
	v_fma_mix_f32 v44, -v174, v41, v163 op_sel_hi:[0,0,1]
	v_mul_f32_e32 v41, v159, v45
	v_fma_mix_f32 v43, -v174, v41, v163 op_sel:[0,0,1] op_sel_hi:[0,0,1]
	v_mul_f32_e32 v41, v159, v46
	v_fma_mix_f32 v42, -v174, v41, v170 op_sel_hi:[0,0,1]
	v_mul_f32_e32 v41, v159, v47
	v_fma_mix_f32 v41, -v174, v41, v170 op_sel:[0,0,1] op_sel_hi:[0,0,1]
	s_waitcnt vmcnt(2)
	v_mov_b32_e32 v163, v212
	s_nop 1
	v_permlane32_swap_b32_e32 v210, v163
	v_mov_b32_e32 v170, v213
	v_fma_mix_f32 v46, -v174, v16, v210 op_sel_hi:[0,0,1]
	v_mul_f32_e32 v16, v159, v17
	v_permlane32_swap_b32_e32 v211, v170
	v_fma_mix_f32 v45, -v174, v16, v210 op_sel:[0,0,1] op_sel_hi:[0,0,1]
	v_mul_f32_e32 v16, v159, v18
	v_fma_mix_f32 v17, -v174, v16, v211 op_sel_hi:[0,0,1]
	v_mul_f32_e32 v16, v159, v19
	v_fma_mix_f32 v16, -v174, v16, v211 op_sel:[0,0,1] op_sel_hi:[0,0,1]
	v_mul_f32_e32 v18, v159, v20
	v_fma_mix_f32 v47, -v174, v18, v163 op_sel_hi:[0,0,1]
	v_mul_f32_e32 v18, v159, v21
	v_fma_mix_f32 v20, -v174, v18, v163 op_sel:[0,0,1] op_sel_hi:[0,0,1]
	v_mul_f32_e32 v18, v159, v22
	v_fma_mix_f32 v19, -v174, v18, v170 op_sel_hi:[0,0,1]
	v_mul_f32_e32 v18, v159, v23
	v_mul_f32_e32 v21, v159, v24
	v_fma_mix_f32 v18, -v174, v18, v170 op_sel:[0,0,1] op_sel_hi:[0,0,1]
	s_waitcnt vmcnt(1)
	v_mov_b32_e32 v163, v216
	s_nop 1
	v_permlane32_swap_b32_e32 v214, v163
	v_mov_b32_e32 v170, v217
	v_fma_mix_f32 v24, -v174, v21, v214 op_sel_hi:[0,0,1]
	v_mul_f32_e32 v21, v159, v25
	v_permlane32_swap_b32_e32 v215, v170
	v_fma_mix_f32 v23, -v174, v21, v214 op_sel:[0,0,1] op_sel_hi:[0,0,1]
	v_mul_f32_e32 v21, v159, v26
	v_fma_mix_f32 v22, -v174, v21, v215 op_sel_hi:[0,0,1]
	v_mul_f32_e32 v21, v159, v27
	v_fma_mix_f32 v21, -v174, v21, v215 op_sel:[0,0,1] op_sel_hi:[0,0,1]
	v_mul_f32_e32 v25, v159, v28
	v_fma_mix_f32 v28, -v174, v25, v163 op_sel_hi:[0,0,1]
	v_mul_f32_e32 v25, v159, v29
	v_fma_mix_f32 v27, -v174, v25, v163 op_sel:[0,0,1] op_sel_hi:[0,0,1]
	v_mul_f32_e32 v25, v159, v30
	v_fma_mix_f32 v26, -v174, v25, v170 op_sel_hi:[0,0,1]
	v_mul_f32_e32 v25, v159, v31
	v_fma_mix_f32 v25, -v174, v25, v170 op_sel:[0,0,1] op_sel_hi:[0,0,1]
	s_waitcnt vmcnt(0)
	v_mov_b32_e32 v170, v220
	s_nop 1
	v_permlane32_swap_b32_e32 v218, v170
	v_mov_b32_e32 v172, v221
	v_fma_mix_f32 v163, -v174, v0, v218 op_sel_hi:[0,0,1]
	v_mul_f32_e32 v0, v159, v1
	v_permlane32_swap_b32_e32 v219, v172
	v_fma_mix_f32 v31, -v174, v0, v218 op_sel:[0,0,1] op_sel_hi:[0,0,1]
	v_mul_f32_e32 v0, v159, v2
	v_fma_mix_f32 v30, -v174, v0, v219 op_sel_hi:[0,0,1]
	v_mul_f32_e32 v0, v159, v3
	v_fma_mix_f32 v29, -v174, v0, v219 op_sel:[0,0,1] op_sel_hi:[0,0,1]
	v_mul_f32_e32 v0, v159, v4
	v_fma_mix_f32 v171, -v174, v0, v170 op_sel_hi:[0,0,1]
	v_mul_f32_e32 v0, v159, v5
	v_fma_mix_f32 v170, -v174, v0, v170 op_sel:[0,0,1] op_sel_hi:[0,0,1]
	v_mul_f32_e32 v0, v159, v6
	v_fma_mix_f32 v5, -v174, v0, v172 op_sel_hi:[0,0,1]
	v_mul_f32_e32 v0, v159, v7
	v_fma_mix_f32 v4, -v174, v0, v172 op_sel:[0,0,1] op_sel_hi:[0,0,1]
	global_load_dwordx4 v[0:3], v162, s[4:5] offset:480
	s_add_u32 s4, s6, s3
	v_readlane_b32 s3, v255, 16
	s_addc_u32 s5, s3, s2
	v_readlane_b32 s2, v255, 28
	s_waitcnt vmcnt(0)
	v_mov_b32_e32 v7, v2
	s_nop 1
	v_permlane32_swap_b32_e32 v0, v7
	v_mul_f32_e32 v2, v159, v8
	v_mov_b32_e32 v162, v3
	v_fma_mix_f32 v6, -v174, v2, v0 op_sel_hi:[0,0,1]
	v_mul_f32_e32 v2, v159, v9
	v_permlane32_swap_b32_e32 v1, v162
	v_fma_mix_f32 v3, -v174, v2, v0 op_sel:[0,0,1] op_sel_hi:[0,0,1]
	v_mul_f32_e32 v0, v159, v10
	v_fma_mix_f32 v2, -v174, v0, v1 op_sel_hi:[0,0,1]
	v_mul_f32_e32 v0, v159, v11
	v_mul_f32_e32 v10, v156, v156
	v_mul_f32_e32 v11, v112, v112
	v_fmac_f32_e32 v10, v157, v157
	v_fmac_f32_e32 v11, v113, v113
	v_fma_mix_f32 v0, -v174, v0, v1 op_sel:[0,0,1] op_sel_hi:[0,0,1]
	v_mul_f32_e32 v1, v159, v12
	v_add_f32_e32 v10, v10, v11
	v_mul_f32_e32 v11, v116, v116
	v_mul_f32_e32 v12, v114, v114
	v_fmac_f32_e32 v11, v158, v158
	v_fmac_f32_e32 v12, v115, v115
	v_fma_mix_f32 v9, -v174, v1, v7 op_sel_hi:[0,0,1]
	v_mul_f32_e32 v1, v159, v13
	v_add_f32_e32 v11, v11, v12
	v_mul_f32_e32 v12, v119, v119
	v_mul_f32_e32 v13, v117, v117
	v_fmac_f32_e32 v12, v120, v120
	v_fmac_f32_e32 v13, v118, v118
	v_fma_mix_f32 v8, -v174, v1, v7 op_sel:[0,0,1] op_sel_hi:[0,0,1]
	v_mul_f32_e32 v1, v159, v14
	v_add_f32_e32 v12, v12, v13
	v_mul_f32_e32 v13, v123, v123
	v_mul_f32_e32 v14, v121, v121
	v_fmac_f32_e32 v13, v124, v124
	v_fmac_f32_e32 v14, v122, v122
	v_add_f32_e32 v13, v13, v14
	v_add_f32_e32 v10, v10, v11
	v_add_f32_e32 v11, v12, v13
	v_add_f32_e32 v10, v10, v11
	v_mul_f32_e32 v11, v125, v125
	v_mul_f32_e32 v12, v96, v96
	v_fmac_f32_e32 v11, v126, v126
	v_fmac_f32_e32 v12, v97, v97
	v_add_f32_e32 v11, v11, v12
	v_mul_f32_e32 v12, v100, v100
	v_mul_f32_e32 v13, v98, v98
	v_fmac_f32_e32 v12, v127, v127
	v_fmac_f32_e32 v13, v99, v99
	v_add_f32_e32 v12, v12, v13
	v_mul_f32_e32 v13, v103, v103
	v_mul_f32_e32 v14, v101, v101
	v_fmac_f32_e32 v13, v104, v104
	v_fmac_f32_e32 v14, v102, v102
	v_fma_mix_f32 v7, -v174, v1, v162 op_sel_hi:[0,0,1]
	v_mul_f32_e32 v1, v159, v15
	v_add_f32_e32 v13, v13, v14
	v_mul_f32_e32 v14, v107, v107
	v_mul_f32_e32 v15, v105, v105
	v_fmac_f32_e32 v14, v108, v108
	v_fmac_f32_e32 v15, v106, v106
	v_add_f32_e32 v14, v14, v15
	v_add_f32_e32 v11, v11, v12
	v_add_f32_e32 v12, v13, v14
	v_add_f32_e32 v11, v11, v12
	v_add_f32_e32 v10, v10, v11
	v_mul_f32_e32 v11, v109, v109
	v_mul_f32_e32 v12, v80, v80
	v_fmac_f32_e32 v11, v110, v110
	v_fmac_f32_e32 v12, v81, v81
	v_add_f32_e32 v11, v11, v12
	v_mul_f32_e32 v12, v84, v84
	v_mul_f32_e32 v13, v82, v82
	v_fmac_f32_e32 v12, v111, v111
	v_fmac_f32_e32 v13, v83, v83
	v_add_f32_e32 v12, v12, v13
	v_mul_f32_e32 v13, v87, v87
	v_mul_f32_e32 v14, v85, v85
	v_fmac_f32_e32 v13, v88, v88
	v_fmac_f32_e32 v14, v86, v86
	v_add_f32_e32 v13, v13, v14
	v_mul_f32_e32 v14, v91, v91
	v_mul_f32_e32 v15, v89, v89
	v_fmac_f32_e32 v14, v92, v92
	v_fmac_f32_e32 v15, v90, v90
	v_add_f32_e32 v14, v14, v15
	v_add_f32_e32 v11, v11, v12
	v_add_f32_e32 v12, v13, v14
	v_add_f32_e32 v11, v11, v12
	v_add_f32_e32 v10, v10, v11
	v_mul_f32_e32 v11, v93, v93
	v_mul_f32_e32 v12, v64, v64
	v_fmac_f32_e32 v11, v94, v94
	v_fmac_f32_e32 v12, v65, v65
	v_add_f32_e32 v11, v11, v12
	v_mul_f32_e32 v12, v68, v68
	v_mul_f32_e32 v13, v66, v66
	v_fmac_f32_e32 v12, v95, v95
	v_fmac_f32_e32 v13, v67, v67
	v_add_f32_e32 v12, v12, v13
	v_mul_f32_e32 v13, v71, v71
	v_mul_f32_e32 v14, v69, v69
	v_fmac_f32_e32 v13, v72, v72
	v_fmac_f32_e32 v14, v70, v70
	v_add_f32_e32 v13, v13, v14
	v_mul_f32_e32 v14, v75, v75
	v_mul_f32_e32 v15, v73, v73
	v_fmac_f32_e32 v14, v76, v76
	v_fmac_f32_e32 v15, v74, v74
	v_add_f32_e32 v14, v14, v15
	v_add_f32_e32 v11, v11, v12
	v_add_f32_e32 v12, v13, v14
	v_add_f32_e32 v11, v11, v12
	v_add_f32_e32 v10, v10, v11
	v_mul_f32_e32 v11, v77, v77
	v_mul_f32_e32 v12, v48, v48
	v_fmac_f32_e32 v11, v78, v78
	v_fmac_f32_e32 v12, v49, v49
	v_add_f32_e32 v11, v11, v12
	v_mul_f32_e32 v12, v52, v52
	v_mul_f32_e32 v13, v50, v50
	v_fmac_f32_e32 v12, v79, v79
	v_fmac_f32_e32 v13, v51, v51
	v_add_f32_e32 v12, v12, v13
	v_mul_f32_e32 v13, v55, v55
	v_mul_f32_e32 v14, v53, v53
	v_fmac_f32_e32 v13, v56, v56
	v_fmac_f32_e32 v14, v54, v54
	v_add_f32_e32 v13, v13, v14
	v_mul_f32_e32 v14, v59, v59
	v_mul_f32_e32 v15, v57, v57
	v_fmac_f32_e32 v14, v60, v60
	v_fmac_f32_e32 v15, v58, v58
	v_add_f32_e32 v14, v14, v15
	v_add_f32_e32 v11, v11, v12
	v_add_f32_e32 v12, v13, v14
	v_add_f32_e32 v11, v11, v12
	v_add_f32_e32 v10, v10, v11
	v_mul_f32_e32 v11, v61, v61
	v_mul_f32_e32 v12, v32, v32
	v_fmac_f32_e32 v11, v62, v62
	v_fmac_f32_e32 v12, v33, v33
	v_add_f32_e32 v11, v11, v12
	v_mul_f32_e32 v12, v36, v36
	v_mul_f32_e32 v13, v34, v34
	v_fmac_f32_e32 v12, v63, v63
	v_fmac_f32_e32 v13, v35, v35
	v_add_f32_e32 v12, v12, v13
	v_mul_f32_e32 v13, v39, v39
	v_mul_f32_e32 v14, v37, v37
	v_fmac_f32_e32 v13, v40, v40
	v_fmac_f32_e32 v14, v38, v38
	v_add_f32_e32 v13, v13, v14
	v_mul_f32_e32 v14, v43, v43
	v_mul_f32_e32 v15, v41, v41
	v_fmac_f32_e32 v14, v44, v44
	v_fmac_f32_e32 v15, v42, v42
	v_add_f32_e32 v14, v14, v15
	v_add_f32_e32 v11, v11, v12
	v_add_f32_e32 v12, v13, v14
	v_add_f32_e32 v11, v11, v12
	v_add_f32_e32 v10, v10, v11
	v_mul_f32_e32 v11, v45, v45
	v_mul_f32_e32 v12, v16, v16
	v_fmac_f32_e32 v11, v46, v46
	v_fmac_f32_e32 v12, v17, v17
	v_add_f32_e32 v11, v11, v12
	v_mul_f32_e32 v12, v20, v20
	v_mul_f32_e32 v13, v18, v18
	v_fmac_f32_e32 v12, v47, v47
	v_fmac_f32_e32 v13, v19, v19
	v_add_f32_e32 v12, v12, v13
	v_mul_f32_e32 v13, v23, v23
	v_mul_f32_e32 v14, v21, v21
	v_fmac_f32_e32 v13, v24, v24
	v_fmac_f32_e32 v14, v22, v22
	v_add_f32_e32 v13, v13, v14
	v_mul_f32_e32 v14, v27, v27
	v_mul_f32_e32 v15, v25, v25
	v_fmac_f32_e32 v14, v28, v28
	v_fmac_f32_e32 v15, v26, v26
	v_add_f32_e32 v14, v14, v15
	v_add_f32_e32 v11, v11, v12
	v_add_f32_e32 v12, v13, v14
	v_add_f32_e32 v11, v11, v12
	v_add_f32_e32 v10, v10, v11
	v_mul_f32_e32 v11, v31, v31
	v_mul_f32_e32 v12, v29, v29
	v_fmac_f32_e32 v11, v163, v163
	v_fmac_f32_e32 v12, v30, v30
	v_add_f32_e32 v11, v11, v12
	v_mul_f32_e32 v12, v170, v170
	v_mul_f32_e32 v13, v4, v4
	v_fmac_f32_e32 v12, v171, v171
	v_fmac_f32_e32 v13, v5, v5
	v_add_f32_e32 v12, v12, v13
	v_mul_f32_e32 v13, v3, v3
	v_mul_f32_e32 v14, v0, v0
	v_fma_mix_f32 v1, -v174, v1, v162 op_sel:[0,0,1] op_sel_hi:[0,0,1]
	v_fmac_f32_e32 v13, v6, v6
	v_fmac_f32_e32 v14, v2, v2
	v_add_f32_e32 v13, v13, v14
	v_mul_f32_e32 v14, v8, v8
	v_mul_f32_e32 v15, v1, v1
	v_fmac_f32_e32 v14, v9, v9
	v_fmac_f32_e32 v15, v7, v7
	v_add_f32_e32 v14, v14, v15
	v_add_f32_e32 v11, v11, v12
	v_add_f32_e32 v12, v13, v14
	v_add_f32_e32 v11, v11, v12
	v_add_f32_e32 v10, v10, v11
	v_mov_b32_e32 v11, v10
	s_nop 1
	v_permlane32_swap_b32_e32 v10, v11
	v_add_f32_e32 v10, v10, v11
	v_fmamk_f32 v10, v10, 0x3b800000, v254
	v_rsq_f32_e32 v10, v10
	v_add_u32_e32 v11, s2, v175
	ds_read_b128 v[12:15], v11
	ds_read_b128 v[176:179], v11 offset:32
	v_readlane_b32 s2, v255, 20
	v_mul_f32_e32 v10, v173, v10
	v_mul_f32_e32 v157, v157, v10
	v_mul_f32_e32 v156, v156, v10
	v_mul_f32_e32 v113, v113, v10
	v_mul_f32_e32 v112, v112, v10
	s_waitcnt lgkmcnt(0)
	v_mul_f32_e32 v12, v12, v157
	v_mul_f32_e32 v157, v158, v10
	v_mul_f32_e32 v13, v13, v156
	v_mul_f32_e32 v116, v116, v10
	v_mul_f32_e32 v14, v14, v113
	v_mul_f32_e32 v113, v115, v10
	v_mul_f32_e32 v15, v15, v112
	v_mul_f32_e32 v112, v114, v10
	v_mul_f32_e32 v157, v176, v157
	v_mul_f32_e32 v116, v177, v116
	v_mul_f32_e32 v113, v178, v113
	v_mul_f32_e32 v112, v179, v112
	v_cvt_pk_bf16_f32 v12, v12, v13
	v_cvt_pk_bf16_f32 v13, v14, v15
	v_cvt_pk_bf16_f32 v14, v157, v116
	v_cvt_pk_bf16_f32 v15, v113, v112
	v_mul_f32_e32 v116, v120, v10
	v_permlane32_swap_b32_e32 v12, v14
	v_permlane32_swap_b32_e32 v13, v15
	global_store_dwordx4 v160, v[12:15], s[4:5]
	ds_read_b128 v[12:15], v11 offset:64
	ds_read_b128 v[112:115], v11 offset:96
	v_mul_f32_e32 v97, v97, v10
	v_mul_f32_e32 v96, v96, v10
	v_mul_f32_e32 v100, v100, v10
	s_waitcnt lgkmcnt(1)
	v_mul_f32_e32 v12, v116, v12
	v_mul_f32_e32 v116, v124, v10
	s_waitcnt lgkmcnt(0)
	v_mul_f32_e32 v112, v116, v112
	v_mul_f32_e32 v116, v119, v10
	v_mul_f32_e32 v13, v116, v13
	v_mul_f32_e32 v116, v123, v10
	v_mul_f32_e32 v113, v116, v113
	v_mul_f32_e32 v116, v118, v10
	v_mul_f32_e32 v14, v116, v14
	v_mul_f32_e32 v116, v122, v10
	v_mul_f32_e32 v114, v116, v114
	v_mul_f32_e32 v116, v117, v10
	v_mul_f32_e32 v15, v116, v15
	v_mul_f32_e32 v116, v121, v10
	v_mul_f32_e32 v115, v116, v115
	v_cvt_pk_bf16_f32 v12, v12, v13
	v_cvt_pk_bf16_f32 v13, v14, v15
	v_cvt_pk_bf16_f32 v14, v112, v113
	v_cvt_pk_bf16_f32 v15, v114, v115
	v_mul_f32_e32 v116, v126, v10
	v_permlane32_swap_b32_e32 v12, v14
	v_permlane32_swap_b32_e32 v13, v15
	global_store_dwordx4 v160, v[12:15], s[4:5] offset:32
	ds_read_b128 v[12:15], v11 offset:128
	ds_read_b128 v[112:115], v11 offset:160
	v_mul_f32_e32 v81, v81, v10
	v_mul_f32_e32 v80, v80, v10
	v_mul_f32_e32 v84, v84, v10
	s_waitcnt lgkmcnt(1)
	v_mul_f32_e32 v12, v116, v12
	v_mul_f32_e32 v116, v127, v10
	s_waitcnt lgkmcnt(0)
	v_mul_f32_e32 v112, v116, v112
	v_mul_f32_e32 v116, v125, v10
	v_mul_f32_e32 v13, v116, v13
	v_mul_f32_e32 v14, v97, v14
	v_mul_f32_e32 v97, v99, v10
	v_mul_f32_e32 v15, v96, v15
	v_mul_f32_e32 v96, v98, v10
	v_mul_f32_e32 v100, v100, v113
	v_mul_f32_e32 v97, v97, v114
	v_mul_f32_e32 v96, v96, v115
	v_cvt_pk_bf16_f32 v12, v12, v13
	v_cvt_pk_bf16_f32 v13, v14, v15
	v_cvt_pk_bf16_f32 v14, v112, v100
	v_cvt_pk_bf16_f32 v15, v97, v96
	v_mul_f32_e32 v100, v104, v10
	v_permlane32_swap_b32_e32 v12, v14
	v_permlane32_swap_b32_e32 v13, v15
	global_store_dwordx4 v160, v[12:15], s[4:5] offset:64
	ds_read_b128 v[12:15], v11 offset:192
	ds_read_b128 v[96:99], v11 offset:224
	v_mul_f32_e32 v65, v65, v10
	v_mul_f32_e32 v64, v64, v10
	v_mul_f32_e32 v68, v68, v10
	s_waitcnt lgkmcnt(1)
	v_mul_f32_e32 v12, v100, v12
	v_mul_f32_e32 v100, v108, v10
	s_waitcnt lgkmcnt(0)
	v_mul_f32_e32 v96, v100, v96
	v_mul_f32_e32 v100, v103, v10
	v_mul_f32_e32 v13, v100, v13
	v_mul_f32_e32 v100, v107, v10
	v_mul_f32_e32 v97, v100, v97
	v_mul_f32_e32 v100, v102, v10
	v_mul_f32_e32 v14, v100, v14
	v_mul_f32_e32 v100, v106, v10
	v_mul_f32_e32 v98, v100, v98
	v_mul_f32_e32 v100, v101, v10
	v_mul_f32_e32 v15, v100, v15
	v_mul_f32_e32 v100, v105, v10
	v_mul_f32_e32 v99, v100, v99
	v_cvt_pk_bf16_f32 v12, v12, v13
	v_cvt_pk_bf16_f32 v13, v14, v15
	v_cvt_pk_bf16_f32 v14, v96, v97
	v_cvt_pk_bf16_f32 v15, v98, v99
	v_or_b32_e32 v96, 64, v160
	v_permlane32_swap_b32_e32 v12, v14
	v_permlane32_swap_b32_e32 v13, v15
	global_store_dwordx4 v96, v[12:15], s[4:5] offset:32
	ds_read_b128 v[12:15], v11 offset:256
	ds_read_b128 v[96:99], v11 offset:288
	v_mul_f32_e32 v100, v110, v10
	v_mul_f32_e32 v49, v49, v10
	v_mul_f32_e32 v48, v48, v10
	s_waitcnt lgkmcnt(1)
	v_mul_f32_e32 v12, v100, v12
	v_mul_f32_e32 v100, v111, v10
	s_waitcnt lgkmcnt(0)
	v_mul_f32_e32 v96, v100, v96
	v_mul_f32_e32 v100, v109, v10
	v_mul_f32_e32 v13, v100, v13
	v_mul_f32_e32 v14, v81, v14
	v_mul_f32_e32 v81, v83, v10
	v_mul_f32_e32 v15, v80, v15
	v_mul_f32_e32 v80, v82, v10
	v_mul_f32_e32 v84, v84, v97
	v_mul_f32_e32 v81, v81, v98
	v_mul_f32_e32 v80, v80, v99
	v_cvt_pk_bf16_f32 v12, v12, v13
	v_cvt_pk_bf16_f32 v13, v14, v15
	v_cvt_pk_bf16_f32 v14, v96, v84
	v_cvt_pk_bf16_f32 v15, v81, v80
	v_mul_f32_e32 v84, v88, v10
	v_permlane32_swap_b32_e32 v12, v14
	v_permlane32_swap_b32_e32 v13, v15
	global_store_dwordx4 v160, v[12:15], s[4:5] offset:128
	ds_read_b128 v[12:15], v11 offset:320
	ds_read_b128 v[80:83], v11 offset:352
	v_mul_f32_e32 v52, v52, v10
	v_mul_f32_e32 v33, v33, v10
	v_mul_f32_e32 v32, v32, v10
	s_waitcnt lgkmcnt(1)
	v_mul_f32_e32 v12, v84, v12
	v_mul_f32_e32 v84, v92, v10
	s_waitcnt lgkmcnt(0)
	v_mul_f32_e32 v80, v84, v80
	v_mul_f32_e32 v84, v87, v10
	v_mul_f32_e32 v13, v84, v13
	v_mul_f32_e32 v84, v91, v10
	v_mul_f32_e32 v81, v84, v81
	v_mul_f32_e32 v84, v86, v10
	v_mul_f32_e32 v14, v84, v14
	v_mul_f32_e32 v84, v90, v10
	v_mul_f32_e32 v82, v84, v82
	v_mul_f32_e32 v84, v85, v10
	v_mul_f32_e32 v15, v84, v15
	v_mul_f32_e32 v84, v89, v10
	v_mul_f32_e32 v83, v84, v83
	v_cvt_pk_bf16_f32 v12, v12, v13
	v_cvt_pk_bf16_f32 v13, v14, v15
	v_cvt_pk_bf16_f32 v14, v80, v81
	v_cvt_pk_bf16_f32 v15, v82, v83
	v_or_b32_e32 v80, 0x80, v160
	v_permlane32_swap_b32_e32 v12, v14
	v_permlane32_swap_b32_e32 v13, v15
	global_store_dwordx4 v80, v[12:15], s[4:5] offset:32
	ds_read_b128 v[12:15], v11 offset:384
	ds_read_b128 v[80:83], v11 offset:416
	v_mul_f32_e32 v84, v94, v10
	v_mul_f32_e32 v36, v36, v10
	v_mul_f32_e32 v17, v17, v10
	s_waitcnt lgkmcnt(1)
	v_mul_f32_e32 v12, v84, v12
	v_mul_f32_e32 v84, v95, v10
	s_waitcnt lgkmcnt(0)
	v_mul_f32_e32 v80, v84, v80
	v_mul_f32_e32 v84, v93, v10
	v_mul_f32_e32 v13, v84, v13
	v_mul_f32_e32 v14, v65, v14
	v_mul_f32_e32 v65, v67, v10
	v_mul_f32_e32 v15, v64, v15
	v_mul_f32_e32 v64, v66, v10
	v_mul_f32_e32 v68, v68, v81
	v_mul_f32_e32 v65, v65, v82
	v_mul_f32_e32 v64, v64, v83
	v_cvt_pk_bf16_f32 v12, v12, v13
	v_cvt_pk_bf16_f32 v13, v14, v15
	v_cvt_pk_bf16_f32 v14, v80, v68
	v_cvt_pk_bf16_f32 v15, v65, v64
	v_mul_f32_e32 v68, v72, v10
	v_permlane32_swap_b32_e32 v12, v14
	v_permlane32_swap_b32_e32 v13, v15
	global_store_dwordx4 v160, v[12:15], s[4:5] offset:192
	ds_read_b128 v[12:15], v11 offset:448
	ds_read_b128 v[64:67], v11 offset:480
	v_mul_f32_e32 v16, v16, v10
	v_mul_f32_e32 v20, v20, v10
	v_mul_f32_e32 v5, v5, v10
	s_waitcnt lgkmcnt(1)
	v_mul_f32_e32 v12, v68, v12
	v_mul_f32_e32 v68, v76, v10
	s_waitcnt lgkmcnt(0)
	v_mul_f32_e32 v64, v68, v64
	v_mul_f32_e32 v68, v71, v10
	v_mul_f32_e32 v13, v68, v13
	v_mul_f32_e32 v68, v75, v10
	v_mul_f32_e32 v65, v68, v65
	v_mul_f32_e32 v68, v70, v10
	v_mul_f32_e32 v14, v68, v14
	v_mul_f32_e32 v68, v74, v10
	v_mul_f32_e32 v66, v68, v66
	v_mul_f32_e32 v68, v69, v10
	v_mul_f32_e32 v15, v68, v15
	v_mul_f32_e32 v68, v73, v10
	v_mul_f32_e32 v67, v68, v67
	v_cvt_pk_bf16_f32 v12, v12, v13
	v_cvt_pk_bf16_f32 v13, v14, v15
	v_cvt_pk_bf16_f32 v14, v64, v65
	v_cvt_pk_bf16_f32 v15, v66, v67
	v_or_b32_e32 v64, 0xc0, v160
	v_permlane32_swap_b32_e32 v12, v14
	v_permlane32_swap_b32_e32 v13, v15
	global_store_dwordx4 v64, v[12:15], s[4:5] offset:32
	ds_read_b128 v[12:15], v11 offset:512
	ds_read_b128 v[64:67], v11 offset:544
	v_mul_f32_e32 v68, v78, v10
	v_mul_f32_e32 v4, v4, v10
	v_mul_f32_e32 v3, v3, v10
	s_waitcnt lgkmcnt(1)
	v_mul_f32_e32 v12, v68, v12
	v_mul_f32_e32 v68, v79, v10
	s_waitcnt lgkmcnt(0)
	v_mul_f32_e32 v64, v68, v64
	v_mul_f32_e32 v68, v77, v10
	v_mul_f32_e32 v13, v68, v13
	v_mul_f32_e32 v14, v49, v14
	v_mul_f32_e32 v49, v51, v10
	v_mul_f32_e32 v15, v48, v15
	v_mul_f32_e32 v48, v50, v10
	v_mul_f32_e32 v52, v52, v65
	v_mul_f32_e32 v49, v49, v66
	v_mul_f32_e32 v48, v48, v67
	v_cvt_pk_bf16_f32 v12, v12, v13
	v_cvt_pk_bf16_f32 v13, v14, v15
	v_cvt_pk_bf16_f32 v14, v64, v52
	v_cvt_pk_bf16_f32 v15, v49, v48
	v_mul_f32_e32 v52, v56, v10
	v_permlane32_swap_b32_e32 v12, v14
	v_permlane32_swap_b32_e32 v13, v15
	global_store_dwordx4 v160, v[12:15], s[4:5] offset:256
	ds_read_b128 v[12:15], v11 offset:576
	ds_read_b128 v[48:51], v11 offset:608
	v_mul_f32_e32 v2, v2, v10
	v_mul_f32_e32 v0, v0, v10
	v_mul_f32_e32 v7, v7, v10
	s_waitcnt lgkmcnt(1)
	v_mul_f32_e32 v12, v52, v12
	v_mul_f32_e32 v52, v60, v10
	s_waitcnt lgkmcnt(0)
	v_mul_f32_e32 v48, v52, v48
	v_mul_f32_e32 v52, v55, v10
	v_mul_f32_e32 v13, v52, v13
	v_mul_f32_e32 v52, v59, v10
	v_mul_f32_e32 v49, v52, v49
	v_mul_f32_e32 v52, v54, v10
	v_mul_f32_e32 v14, v52, v14
	v_mul_f32_e32 v52, v58, v10
	v_mul_f32_e32 v50, v52, v50
	v_mul_f32_e32 v52, v53, v10
	v_mul_f32_e32 v15, v52, v15
	v_mul_f32_e32 v52, v57, v10
	v_mul_f32_e32 v51, v52, v51
	v_cvt_pk_bf16_f32 v12, v12, v13
	v_cvt_pk_bf16_f32 v13, v14, v15
	v_cvt_pk_bf16_f32 v14, v48, v49
	v_cvt_pk_bf16_f32 v15, v50, v51
	v_or_b32_e32 v48, 0x100, v160
	v_permlane32_swap_b32_e32 v12, v14
	v_permlane32_swap_b32_e32 v13, v15
	global_store_dwordx4 v48, v[12:15], s[4:5] offset:32
	ds_read_b128 v[12:15], v11 offset:640
	ds_read_b128 v[48:51], v11 offset:672
	v_mul_f32_e32 v52, v62, v10
	s_cmp_lt_u32 s94, s2
	s_waitcnt lgkmcnt(1)
	v_mul_f32_e32 v12, v52, v12
	v_mul_f32_e32 v52, v63, v10
	s_waitcnt lgkmcnt(0)
	v_mul_f32_e32 v48, v52, v48
	v_mul_f32_e32 v52, v61, v10
	v_mul_f32_e32 v13, v52, v13
	v_mul_f32_e32 v14, v33, v14
	v_mul_f32_e32 v33, v35, v10
	v_mul_f32_e32 v15, v32, v15
	v_mul_f32_e32 v32, v34, v10
	v_mul_f32_e32 v36, v36, v49
	v_mul_f32_e32 v33, v33, v50
	v_mul_f32_e32 v32, v32, v51
	v_cvt_pk_bf16_f32 v12, v12, v13
	v_cvt_pk_bf16_f32 v13, v14, v15
	v_cvt_pk_bf16_f32 v14, v48, v36
	v_cvt_pk_bf16_f32 v15, v33, v32
	v_mul_f32_e32 v36, v40, v10
	v_permlane32_swap_b32_e32 v12, v14
	v_permlane32_swap_b32_e32 v13, v15
	global_store_dwordx4 v160, v[12:15], s[4:5] offset:320
	ds_read_b128 v[12:15], v11 offset:704
	ds_read_b128 v[32:35], v11 offset:736
	s_waitcnt lgkmcnt(1)
	v_mul_f32_e32 v12, v36, v12
	v_mul_f32_e32 v36, v44, v10
	s_waitcnt lgkmcnt(0)
	v_mul_f32_e32 v32, v36, v32
	v_mul_f32_e32 v36, v39, v10
	v_mul_f32_e32 v13, v36, v13
	v_mul_f32_e32 v36, v43, v10
	v_mul_f32_e32 v33, v36, v33
	v_mul_f32_e32 v36, v38, v10
	v_mul_f32_e32 v14, v36, v14
	v_mul_f32_e32 v36, v42, v10
	v_mul_f32_e32 v34, v36, v34
	v_mul_f32_e32 v36, v37, v10
	v_mul_f32_e32 v15, v36, v15
	v_mul_f32_e32 v36, v41, v10
	v_mul_f32_e32 v35, v36, v35
	v_cvt_pk_bf16_f32 v12, v12, v13
	v_cvt_pk_bf16_f32 v13, v14, v15
	v_cvt_pk_bf16_f32 v14, v32, v33
	v_cvt_pk_bf16_f32 v15, v34, v35
	v_or_b32_e32 v32, 0x140, v160
	v_permlane32_swap_b32_e32 v12, v14
	v_permlane32_swap_b32_e32 v13, v15
	global_store_dwordx4 v32, v[12:15], s[4:5] offset:32
	ds_read_b128 v[12:15], v11 offset:768
	ds_read_b128 v[32:35], v11 offset:800
	v_mul_f32_e32 v36, v46, v10
	s_waitcnt lgkmcnt(1)
	v_mul_f32_e32 v12, v36, v12
	v_mul_f32_e32 v36, v47, v10
	s_waitcnt lgkmcnt(0)
	v_mul_f32_e32 v32, v36, v32
	v_mul_f32_e32 v36, v45, v10
	v_mul_f32_e32 v13, v36, v13
	v_mul_f32_e32 v14, v17, v14
	v_mul_f32_e32 v17, v19, v10
	v_mul_f32_e32 v15, v16, v15
	v_mul_f32_e32 v16, v18, v10
	v_mul_f32_e32 v20, v20, v33
	v_mul_f32_e32 v17, v17, v34
	v_mul_f32_e32 v16, v16, v35
	v_cvt_pk_bf16_f32 v12, v12, v13
	v_cvt_pk_bf16_f32 v13, v14, v15
	v_cvt_pk_bf16_f32 v14, v32, v20
	v_cvt_pk_bf16_f32 v15, v17, v16
	v_mul_f32_e32 v20, v24, v10
	v_permlane32_swap_b32_e32 v12, v14
	v_permlane32_swap_b32_e32 v13, v15
	global_store_dwordx4 v160, v[12:15], s[4:5] offset:384
	ds_read_b128 v[12:15], v11 offset:832
	ds_read_b128 v[16:19], v11 offset:864
	s_waitcnt lgkmcnt(1)
	v_mul_f32_e32 v12, v20, v12
	v_mul_f32_e32 v20, v28, v10
	s_waitcnt lgkmcnt(0)
	v_mul_f32_e32 v16, v20, v16
	v_mul_f32_e32 v20, v23, v10
	v_mul_f32_e32 v13, v20, v13
	v_mul_f32_e32 v20, v27, v10
	v_mul_f32_e32 v17, v20, v17
	v_mul_f32_e32 v20, v22, v10
	v_mul_f32_e32 v14, v20, v14
	v_mul_f32_e32 v20, v26, v10
	v_mul_f32_e32 v18, v20, v18
	v_mul_f32_e32 v20, v21, v10
	v_mul_f32_e32 v15, v20, v15
	v_mul_f32_e32 v20, v25, v10
	v_mul_f32_e32 v19, v20, v19
	v_cvt_pk_bf16_f32 v12, v12, v13
	v_cvt_pk_bf16_f32 v13, v14, v15
	v_cvt_pk_bf16_f32 v14, v16, v17
	v_cvt_pk_bf16_f32 v15, v18, v19
	v_or_b32_e32 v16, 0x180, v160
	v_permlane32_swap_b32_e32 v12, v14
	v_permlane32_swap_b32_e32 v13, v15
	global_store_dwordx4 v16, v[12:15], s[4:5] offset:32
	ds_read_b128 v[12:15], v11 offset:896
	ds_read_b128 v[16:19], v11 offset:928
	v_mul_f32_e32 v20, v163, v10
	s_waitcnt lgkmcnt(1)
	v_mul_f32_e32 v12, v20, v12
	v_mul_f32_e32 v20, v171, v10
	s_waitcnt lgkmcnt(0)
	v_mul_f32_e32 v16, v20, v16
	v_mul_f32_e32 v20, v31, v10
	v_mul_f32_e32 v13, v20, v13
	v_mul_f32_e32 v20, v170, v10
	v_mul_f32_e32 v17, v20, v17
	v_mul_f32_e32 v20, v30, v10
	v_mul_f32_e32 v5, v5, v18
	v_mul_f32_e32 v18, v29, v10
	v_mul_f32_e32 v14, v20, v14
	v_mul_f32_e32 v15, v18, v15
	v_mul_f32_e32 v4, v4, v19
	v_cvt_pk_bf16_f32 v12, v12, v13
	v_cvt_pk_bf16_f32 v13, v14, v15
	v_cvt_pk_bf16_f32 v14, v16, v17
	v_cvt_pk_bf16_f32 v15, v5, v4
	v_mul_f32_e32 v4, v6, v10
	v_permlane32_swap_b32_e32 v12, v14
	v_permlane32_swap_b32_e32 v13, v15
	global_store_dwordx4 v160, v[12:15], s[4:5] offset:448
	ds_read_b128 v[12:15], v11 offset:960
	ds_read_b128 v[16:19], v11 offset:992
	v_mul_f32_e32 v5, v9, v10
	v_mul_f32_e32 v6, v8, v10
	s_waitcnt lgkmcnt(1)
	v_mul_f32_e32 v3, v3, v13
	v_mul_f32_e32 v2, v2, v14
	v_mul_f32_e32 v8, v0, v15
	v_mul_f32_e32 v0, v1, v10
	v_mul_f32_e32 v4, v4, v12
	s_waitcnt lgkmcnt(0)
	v_mul_f32_e32 v5, v5, v16
	v_mul_f32_e32 v6, v6, v17
	v_mul_f32_e32 v7, v7, v18
	v_mul_f32_e32 v9, v0, v19
	v_cvt_pk_bf16_f32 v0, v4, v3
	v_cvt_pk_bf16_f32 v1, v2, v8
	v_cvt_pk_bf16_f32 v2, v5, v6
	v_cvt_pk_bf16_f32 v3, v7, v9
	v_or_b32_e32 v4, 0x1c0, v160
	v_permlane32_swap_b32_e32 v0, v2
	v_permlane32_swap_b32_e32 v1, v3
	global_store_dwordx4 v4, v[0:3], s[4:5] offset:32
	s_cbranch_scc0 .LBB0_616
